# speedup vs baseline: 1.0299x; 1.0010x over previous
_Z8gat_mainPKiPKDF16_PKfS4_Pf:
	s_load_dwordx8 s[24:31], s[0:1], 0x0
	s_load_dwordx2 s[12:13], s[0:1], 0x20
	v_and_b32_e32 v2, 63, v0
	v_readfirstlane_b32 s16, v0
	v_lshlrev_b32_e32 v1, 4, v2
	s_lshr_b32 s16, s16, 6
	s_and_b32 s17, s2, 7
	s_lshr_b32 s18, s2, 3
	s_lshr_b32 s19, s18, 3
	s_add_u32 s19, s19, s18
	s_and_b32 s19, s19, 7
	s_lshr_b32 s20, s16, 2
	s_and_b32 s21, s16, 3
	s_lshl_b32 s22, s16, 16
	s_lshl_b32 s23, s16, 12
	s_waitcnt lgkmcnt(0)
	s_lshl_b32 s3, s17, 24
	s_lshl_b32 s57, s18, 19
	s_add_u32 s3, s3, s57
	s_add_u32 s4, s24, s3
	s_addc_u32 s5, s25, 0
	s_and_b32 s5, s5, 0xffff
	s_mov_b32 s6, 0x80000
	s_mov_b32 s7, 0x20000
	s_lshl_b32 s3, s17, 18
	s_add_u32 s8, s26, s3
	s_addc_u32 s9, s27, 0
	s_and_b32 s9, s9, 0xffff
	s_mov_b32 s10, 0x40000
	s_mov_b32 s11, 0x20000
	s_lshl_b32 s3, s17, 11
	s_lshl_b32 s57, s18, 6
	s_add_u32 s3, s3, s57
	s_lshl_b32 s57, s16, 3
	s_add_u32 s3, s3, s57
	s_lshl_b32 s3, s3, 2
	s_add_u32 s28, s28, s3
	s_addc_u32 s29, s29, 0
	v_and_b32_e32 v36, 7, v0
	v_lshlrev_b32_e32 v36, 2, v36
	global_load_dword v37, v36, s[28:29]
	s_lshl_b32 s3, s17, 13
	s_add_u32 s30, s30, s3
	s_addc_u32 s31, s31, 0
	v_lshlrev_b32_e32 v38, 4, v0
	global_load_dwordx4 v[24:27], v38, s[30:31]
	s_add_u32 s3, s19, 0
	s_and_b32 s3, s3, 7
	s_lshl_b32 s57, s3, 10
	s_add_u32 s48, s57, s22
	s_add_u32 s49, s48, 0x2000
	s_add_u32 s50, s48, 0x4000
	s_add_u32 s51, s48, 0x6000
	s_add_u32 s52, s48, 0x8000
	s_add_u32 s53, s48, 0xa000
	s_add_u32 s54, s48, 0xc000
	s_add_u32 s55, s48, 0xe000
	s_lshl_b32 s56, s3, 15
	s_add_u32 s56, s56, s23
	buffer_load_dwordx4 v[88:91], v1, s[4:7], s48 offen nt
	buffer_load_dwordx4 v[92:95], v1, s[4:7], s49 offen nt
	buffer_load_dwordx4 v[96:99], v1, s[4:7], s50 offen nt
	buffer_load_dwordx4 v[100:103], v1, s[4:7], s51 offen nt
	buffer_load_dwordx4 v[104:107], v1, s[4:7], s52 offen nt
	buffer_load_dwordx4 v[108:111], v1, s[4:7], s53 offen nt
	buffer_load_dwordx4 v[112:115], v1, s[4:7], s54 offen nt
	buffer_load_dwordx4 v[116:119], v1, s[4:7], s55 offen nt
	buffer_load_dwordx4 v[152:155], v1, s[8:11], s56 offen
	buffer_load_dwordx4 v[156:159], v1, s[8:11], s56 offen offset:1024
	buffer_load_dwordx4 v[160:163], v1, s[8:11], s56 offen offset:2048
	buffer_load_dwordx4 v[164:167], v1, s[8:11], s56 offen offset:3072
	s_mul_i32 s3, s16, 0x1080
	v_lshlrev_b32_e32 v3, 3, v2
	v_add_u32_e32 v3, s3, v3
	v_add_u32_e32 v4, 0x840, v3
	v_add_u32_e32 v5, 0x8400, v3
	v_add_u32_e32 v6, 0x8400, v4
	v_and_b32_e32 v36, 31, v2
	v_mul_u32_u24_e32 v36, 0x210, v36
	v_lshrrev_b32_e32 v38, 5, v2
	v_lshlrev_b32_e32 v38, 4, v38
	v_add_u32_e32 v7, v36, v38
	s_mul_i32 s3, s20, 0x4200
	s_lshl_b32 s57, s21, 7
	s_add_u32 s3, s3, s57
	v_add_u32_e32 v7, s3, v7
	s_lshl_b32 s3, s21, 13
	s_add_u32 s3, s3, 0x14800
	v_add_u32_e32 v8, s3, v1
	s_add_u32 s3, s23, 0x14800
	v_add_u32_e32 v9, s3, v1
	v_add_u32_e32 v10, 0x10800, v1
	v_mov_b32_e32 v12, 0x3c003c00
	v_mov_b32_e32 v13, 0x3c003c00
	v_mov_b32_e32 v14, 0x3c003c00
	v_mov_b32_e32 v15, 0x3c003c00
	v_mov_b32_e32 v40, 0
	v_mov_b32_e32 v41, 0
	v_mov_b32_e32 v42, 0
	v_mov_b32_e32 v43, 0
	v_mov_b32_e32 v44, 0
	v_mov_b32_e32 v45, 0
	v_mov_b32_e32 v46, 0
	v_mov_b32_e32 v47, 0
	v_mov_b32_e32 v48, 0
	v_mov_b32_e32 v49, 0
	v_mov_b32_e32 v50, 0
	v_mov_b32_e32 v51, 0
	v_mov_b32_e32 v52, 0
	v_mov_b32_e32 v53, 0
	v_mov_b32_e32 v54, 0
	v_mov_b32_e32 v55, 0
	v_mov_b32_e32 v56, 0
	v_mov_b32_e32 v57, 0
	v_mov_b32_e32 v58, 0
	v_mov_b32_e32 v59, 0
	v_mov_b32_e32 v60, 0
	v_mov_b32_e32 v61, 0
	v_mov_b32_e32 v62, 0
	v_mov_b32_e32 v63, 0
	v_mov_b32_e32 v64, 0
	v_mov_b32_e32 v65, 0
	v_mov_b32_e32 v66, 0
	v_mov_b32_e32 v67, 0
	v_mov_b32_e32 v68, 0
	v_mov_b32_e32 v69, 0
	v_mov_b32_e32 v70, 0
	v_mov_b32_e32 v71, 0
	v_mov_b32_e32 v72, 0
	v_mov_b32_e32 v73, 0
	v_mov_b32_e32 v74, 0
	v_mov_b32_e32 v75, 0
	v_mov_b32_e32 v76, 0
	v_mov_b32_e32 v77, 0
	v_mov_b32_e32 v78, 0
	v_mov_b32_e32 v79, 0
	v_mov_b32_e32 v80, 0
	v_mov_b32_e32 v81, 0
	v_mov_b32_e32 v82, 0
	v_mov_b32_e32 v83, 0
	v_mov_b32_e32 v84, 0
	v_mov_b32_e32 v85, 0
	v_mov_b32_e32 v86, 0
	v_mov_b32_e32 v87, 0
	s_lshl_b32 s3, s17, 11
	s_lshl_b32 s57, s18, 6
	s_add_u32 s3, s3, s57
	s_lshl_b32 s57, s20, 5
	s_add_u32 s3, s3, s57
	s_lshl_b32 s57, s21, 3
	s_add_u32 s3, s3, s57
	s_lshl_b32 s3, s3, 8
	s_add_u32 s12, s12, s3
	s_addc_u32 s13, s13, 0
	s_waitcnt vmcnt(12)
	v_max_f32_e32 v28, v24, v25
	v_max3_f32 v28, v28, v26, v27
	v_lshlrev_b32_e32 v29, 2, v2
	v_xor_b32_e32 v30, 4, v29
	ds_bpermute_b32 v31, v30, v28
	s_waitcnt lgkmcnt(0)
	v_max_f32_e32 v28, v28, v31
	v_xor_b32_e32 v30, 8, v29
	ds_bpermute_b32 v31, v30, v28
	s_waitcnt lgkmcnt(0)
	v_max_f32_e32 v28, v28, v31
	v_xor_b32_e32 v30, 16, v29
	ds_bpermute_b32 v31, v30, v28
	s_waitcnt lgkmcnt(0)
	v_max_f32_e32 v28, v28, v31
	v_xor_b32_e32 v30, 32, v29
	ds_bpermute_b32 v31, v30, v28
	s_waitcnt lgkmcnt(0)
	v_max_f32_e32 v28, v28, v31
	v_xor_b32_e32 v30, 64, v29
	ds_bpermute_b32 v31, v30, v28
	s_waitcnt lgkmcnt(0)
	v_max_f32_e32 v28, v28, v31
	v_xor_b32_e32 v30, 128, v29
	ds_bpermute_b32 v31, v30, v28
	s_waitcnt lgkmcnt(0)
	v_max_f32_e32 v28, v28, v31
	s_lshl_b32 s3, s16, 2
	s_add_u32 s3, s3, 0x24800
	v_mov_b32_e32 v30, s3
	ds_write_b32 v30, v28
	s_waitcnt lgkmcnt(0)
	s_barrier
	v_mov_b32_e32 v30, 0x24800
	ds_read_b128 v[32:35], v30
	ds_read_b128 v[16:19], v30 offset:16
	s_waitcnt lgkmcnt(0)
	v_max3_f32 v28, v32, v33, v34
	v_max3_f32 v28, v28, v35, v16
	v_max3_f32 v28, v28, v17, v18
	v_max_f32_e32 v28, v28, v19
	v_sub_f32_e32 v16, v24, v28
	v_sub_f32_e32 v17, v25, v28
	v_sub_f32_e32 v18, v26, v28
	v_sub_f32_e32 v19, v27, v28
	v_mul_f32_e32 v20, 0x3e4ccccd, v16
	v_mul_f32_e32 v21, 0x3e4ccccd, v17
	v_mul_f32_e32 v22, 0x3e4ccccd, v18
	v_mul_f32_e32 v23, 0x3e4ccccd, v19
	v_exp_f32_e32 v16, v16
	v_exp_f32_e32 v17, v17
	v_exp_f32_e32 v18, v18
	v_exp_f32_e32 v19, v19
	v_exp_f32_e32 v20, v20
	v_exp_f32_e32 v21, v21
	v_exp_f32_e32 v22, v22
	v_exp_f32_e32 v23, v23
	v_lshlrev_b32_e32 v30, 4, v0
	v_add_u32_e32 v30, 0x10800, v30
	ds_write_b128 v30, v[16:19]
	ds_write_b128 v30, v[20:23] offset:8192
	v_add_f32_e32 v36, v37, v28
	v_mul_f32_e32 v38, 0x3e4ccccd, v36
	v_max_f32_e32 v39, v36, v38
	v_sub_f32_e32 v36, v36, v39
	v_sub_f32_e32 v38, v38, v39
	v_add_f32_e32 v36, 0x41600000, v36
	v_add_f32_e32 v38, 0x41600000, v38
	v_exp_f32_e32 v36, v36
	v_exp_f32_e32 v38, v38
	s_nop 1
	v_readlane_b32 s32, v36, 0
	v_readlane_b32 s33, v36, 1
	v_readlane_b32 s34, v36, 2
	v_readlane_b32 s35, v36, 3
	v_readlane_b32 s36, v36, 4
	v_readlane_b32 s37, v36, 5
	v_readlane_b32 s38, v36, 6
	v_readlane_b32 s39, v36, 7
	v_readlane_b32 s40, v38, 0
	v_readlane_b32 s41, v38, 1
	v_readlane_b32 s42, v38, 2
	v_readlane_b32 s43, v38, 3
	v_readlane_b32 s44, v38, 4
	v_readlane_b32 s45, v38, 5
	v_readlane_b32 s46, v38, 6
	v_readlane_b32 s47, v38, 7
	s_waitcnt lgkmcnt(0)
	s_barrier
	s_lshl_b32 s3, s19, 10
	v_add_u32_e32 v11, s3, v10
	ds_read_b128 v[16:19], v11
	ds_read_b128 v[20:23], v11 offset:8192
	s_waitcnt lgkmcnt(0)
	s_add_u32 s3, s19, 1
	s_and_b32 s3, s3, 7
	s_lshl_b32 s57, s3, 10
	s_add_u32 s48, s57, s22
	s_add_u32 s49, s48, 0x2000
	s_add_u32 s50, s48, 0x4000
	s_add_u32 s51, s48, 0x6000
	s_add_u32 s52, s48, 0x8000
	s_add_u32 s53, s48, 0xa000
	s_add_u32 s54, s48, 0xc000
	s_add_u32 s55, s48, 0xe000
	s_lshl_b32 s56, s3, 15
	s_add_u32 s56, s56, s23
	buffer_load_dwordx4 v[120:123], v1, s[4:7], s48 offen nt
	buffer_load_dwordx4 v[124:127], v1, s[4:7], s49 offen nt
	buffer_load_dwordx4 v[128:131], v1, s[4:7], s50 offen nt
	buffer_load_dwordx4 v[132:135], v1, s[4:7], s51 offen nt
	buffer_load_dwordx4 v[136:139], v1, s[4:7], s52 offen nt
	buffer_load_dwordx4 v[140:143], v1, s[4:7], s53 offen nt
	buffer_load_dwordx4 v[144:147], v1, s[4:7], s54 offen nt
	buffer_load_dwordx4 v[148:151], v1, s[4:7], s55 offen nt
	buffer_load_dwordx4 v[168:171], v1, s[8:11], s56 offen
	buffer_load_dwordx4 v[172:175], v1, s[8:11], s56 offen offset:1024
	buffer_load_dwordx4 v[176:179], v1, s[8:11], s56 offen offset:2048
	buffer_load_dwordx4 v[180:183], v1, s[8:11], s56 offen offset:3072
	s_waitcnt vmcnt(12)
	v_pk_mul_f32 v[24:25], v[16:17], s[32:33] op_sel_hi:[1,0]
	v_pk_mul_f32 v[26:27], v[18:19], s[32:33] op_sel_hi:[1,0]
	v_pk_mul_f32 v[28:29], v[20:21], s[40:41] op_sel_hi:[1,0]
	v_pk_mul_f32 v[30:31], v[22:23], s[40:41] op_sel_hi:[1,0]
	v_cmp_lt_i32_e64 s[60:61], 0, v88
	v_cmp_lt_i32_e64 s[62:63], 0, v89
	v_cmp_lt_i32_e64 s[64:65], 0, v90
	v_cmp_lt_i32_e64 s[66:67], 0, v91
	v_max_f32_e32 v24, v24, v28
	v_max_f32_e32 v25, v25, v29
	v_max_f32_e32 v26, v26, v30
	v_max_f32_e32 v27, v27, v31
	v_cndmask_b32_e64 v24, 0, v24, s[60:61]
	v_cndmask_b32_e64 v25, 0, v25, s[62:63]
	v_cndmask_b32_e64 v26, 0, v26, s[64:65]
	v_cndmask_b32_e64 v27, 0, v27, s[66:67]
	v_cvt_pkrtz_f16_f32 v32, v24, v25
	v_cvt_pkrtz_f16_f32 v33, v26, v27
	v_pk_mul_f32 v[24:25], v[16:17], s[32:33] op_sel:[0,1] op_sel_hi:[1,1]
	v_pk_mul_f32 v[26:27], v[18:19], s[32:33] op_sel:[0,1] op_sel_hi:[1,1]
	v_pk_mul_f32 v[28:29], v[20:21], s[40:41] op_sel:[0,1] op_sel_hi:[1,1]
	v_pk_mul_f32 v[30:31], v[22:23], s[40:41] op_sel:[0,1] op_sel_hi:[1,1]
	v_cmp_lt_i32_e64 s[60:61], 0, v92
	v_cmp_lt_i32_e64 s[62:63], 0, v93
	v_cmp_lt_i32_e64 s[64:65], 0, v94
	v_cmp_lt_i32_e64 s[66:67], 0, v95
	v_max_f32_e32 v24, v24, v28
	v_max_f32_e32 v25, v25, v29
	v_max_f32_e32 v26, v26, v30
	v_max_f32_e32 v27, v27, v31
	v_cndmask_b32_e64 v24, 0, v24, s[60:61]
	v_cndmask_b32_e64 v25, 0, v25, s[62:63]
	v_cndmask_b32_e64 v26, 0, v26, s[64:65]
	v_cndmask_b32_e64 v27, 0, v27, s[66:67]
	v_cvt_pkrtz_f16_f32 v34, v24, v25
	v_cvt_pkrtz_f16_f32 v35, v26, v27
	ds_write2_b64 v3, v[32:33], v[34:35] offset0:0 offset1:66
	v_pk_mul_f32 v[24:25], v[16:17], s[34:35] op_sel_hi:[1,0]
	v_pk_mul_f32 v[26:27], v[18:19], s[34:35] op_sel_hi:[1,0]
	v_pk_mul_f32 v[28:29], v[20:21], s[42:43] op_sel_hi:[1,0]
	v_pk_mul_f32 v[30:31], v[22:23], s[42:43] op_sel_hi:[1,0]
	v_cmp_lt_i32_e64 s[60:61], 0, v96
	v_cmp_lt_i32_e64 s[62:63], 0, v97
	v_cmp_lt_i32_e64 s[64:65], 0, v98
	v_cmp_lt_i32_e64 s[66:67], 0, v99
	v_max_f32_e32 v24, v24, v28
	v_max_f32_e32 v25, v25, v29
	v_max_f32_e32 v26, v26, v30
	v_max_f32_e32 v27, v27, v31
	v_cndmask_b32_e64 v24, 0, v24, s[60:61]
	v_cndmask_b32_e64 v25, 0, v25, s[62:63]
	v_cndmask_b32_e64 v26, 0, v26, s[64:65]
	v_cndmask_b32_e64 v27, 0, v27, s[66:67]
	v_cvt_pkrtz_f16_f32 v32, v24, v25
	v_cvt_pkrtz_f16_f32 v33, v26, v27
	v_pk_mul_f32 v[24:25], v[16:17], s[34:35] op_sel:[0,1] op_sel_hi:[1,1]
	v_pk_mul_f32 v[26:27], v[18:19], s[34:35] op_sel:[0,1] op_sel_hi:[1,1]
	v_pk_mul_f32 v[28:29], v[20:21], s[42:43] op_sel:[0,1] op_sel_hi:[1,1]
	v_pk_mul_f32 v[30:31], v[22:23], s[42:43] op_sel:[0,1] op_sel_hi:[1,1]
	v_cmp_lt_i32_e64 s[60:61], 0, v100
	v_cmp_lt_i32_e64 s[62:63], 0, v101
	v_cmp_lt_i32_e64 s[64:65], 0, v102
	v_cmp_lt_i32_e64 s[66:67], 0, v103
	v_max_f32_e32 v24, v24, v28
	v_max_f32_e32 v25, v25, v29
	v_max_f32_e32 v26, v26, v30
	v_max_f32_e32 v27, v27, v31
	v_cndmask_b32_e64 v24, 0, v24, s[60:61]
	v_cndmask_b32_e64 v25, 0, v25, s[62:63]
	v_cndmask_b32_e64 v26, 0, v26, s[64:65]
	v_cndmask_b32_e64 v27, 0, v27, s[66:67]
	v_cvt_pkrtz_f16_f32 v34, v24, v25
	v_cvt_pkrtz_f16_f32 v35, v26, v27
	ds_write2_b64 v3, v[32:33], v[34:35] offset0:132 offset1:198
	v_pk_mul_f32 v[24:25], v[16:17], s[36:37] op_sel_hi:[1,0]
	v_pk_mul_f32 v[26:27], v[18:19], s[36:37] op_sel_hi:[1,0]
	v_pk_mul_f32 v[28:29], v[20:21], s[44:45] op_sel_hi:[1,0]
	v_pk_mul_f32 v[30:31], v[22:23], s[44:45] op_sel_hi:[1,0]
	v_cmp_lt_i32_e64 s[60:61], 0, v104
	v_cmp_lt_i32_e64 s[62:63], 0, v105
	v_cmp_lt_i32_e64 s[64:65], 0, v106
	v_cmp_lt_i32_e64 s[66:67], 0, v107
	v_max_f32_e32 v24, v24, v28
	v_max_f32_e32 v25, v25, v29
	v_max_f32_e32 v26, v26, v30
	v_max_f32_e32 v27, v27, v31
	v_cndmask_b32_e64 v24, 0, v24, s[60:61]
	v_cndmask_b32_e64 v25, 0, v25, s[62:63]
	v_cndmask_b32_e64 v26, 0, v26, s[64:65]
	v_cndmask_b32_e64 v27, 0, v27, s[66:67]
	v_cvt_pkrtz_f16_f32 v32, v24, v25
	v_cvt_pkrtz_f16_f32 v33, v26, v27
	v_pk_mul_f32 v[24:25], v[16:17], s[36:37] op_sel:[0,1] op_sel_hi:[1,1]
	v_pk_mul_f32 v[26:27], v[18:19], s[36:37] op_sel:[0,1] op_sel_hi:[1,1]
	v_pk_mul_f32 v[28:29], v[20:21], s[44:45] op_sel:[0,1] op_sel_hi:[1,1]
	v_pk_mul_f32 v[30:31], v[22:23], s[44:45] op_sel:[0,1] op_sel_hi:[1,1]
	v_cmp_lt_i32_e64 s[60:61], 0, v108
	v_cmp_lt_i32_e64 s[62:63], 0, v109
	v_cmp_lt_i32_e64 s[64:65], 0, v110
	v_cmp_lt_i32_e64 s[66:67], 0, v111
	v_max_f32_e32 v24, v24, v28
	v_max_f32_e32 v25, v25, v29
	v_max_f32_e32 v26, v26, v30
	v_max_f32_e32 v27, v27, v31
	v_cndmask_b32_e64 v24, 0, v24, s[60:61]
	v_cndmask_b32_e64 v25, 0, v25, s[62:63]
	v_cndmask_b32_e64 v26, 0, v26, s[64:65]
	v_cndmask_b32_e64 v27, 0, v27, s[66:67]
	v_cvt_pkrtz_f16_f32 v34, v24, v25
	v_cvt_pkrtz_f16_f32 v35, v26, v27
	ds_write2_b64 v4, v[32:33], v[34:35] offset0:0 offset1:66
	v_pk_mul_f32 v[24:25], v[16:17], s[38:39] op_sel_hi:[1,0]
	v_pk_mul_f32 v[26:27], v[18:19], s[38:39] op_sel_hi:[1,0]
	v_pk_mul_f32 v[28:29], v[20:21], s[46:47] op_sel_hi:[1,0]
	v_pk_mul_f32 v[30:31], v[22:23], s[46:47] op_sel_hi:[1,0]
	v_cmp_lt_i32_e64 s[60:61], 0, v112
	v_cmp_lt_i32_e64 s[62:63], 0, v113
	v_cmp_lt_i32_e64 s[64:65], 0, v114
	v_cmp_lt_i32_e64 s[66:67], 0, v115
	v_max_f32_e32 v24, v24, v28
	v_max_f32_e32 v25, v25, v29
	v_max_f32_e32 v26, v26, v30
	v_max_f32_e32 v27, v27, v31
	v_cndmask_b32_e64 v24, 0, v24, s[60:61]
	v_cndmask_b32_e64 v25, 0, v25, s[62:63]
	v_cndmask_b32_e64 v26, 0, v26, s[64:65]
	v_cndmask_b32_e64 v27, 0, v27, s[66:67]
	v_cvt_pkrtz_f16_f32 v32, v24, v25
	v_cvt_pkrtz_f16_f32 v33, v26, v27
	v_pk_mul_f32 v[24:25], v[16:17], s[38:39] op_sel:[0,1] op_sel_hi:[1,1]
	v_pk_mul_f32 v[26:27], v[18:19], s[38:39] op_sel:[0,1] op_sel_hi:[1,1]
	v_pk_mul_f32 v[28:29], v[20:21], s[46:47] op_sel:[0,1] op_sel_hi:[1,1]
	v_pk_mul_f32 v[30:31], v[22:23], s[46:47] op_sel:[0,1] op_sel_hi:[1,1]
	v_cmp_lt_i32_e64 s[60:61], 0, v116
	v_cmp_lt_i32_e64 s[62:63], 0, v117
	v_cmp_lt_i32_e64 s[64:65], 0, v118
	v_cmp_lt_i32_e64 s[66:67], 0, v119
	v_max_f32_e32 v24, v24, v28
	v_max_f32_e32 v25, v25, v29
	v_max_f32_e32 v26, v26, v30
	v_max_f32_e32 v27, v27, v31
	v_cndmask_b32_e64 v24, 0, v24, s[60:61]
	v_cndmask_b32_e64 v25, 0, v25, s[62:63]
	v_cndmask_b32_e64 v26, 0, v26, s[64:65]
	v_cndmask_b32_e64 v27, 0, v27, s[66:67]
	v_cvt_pkrtz_f16_f32 v34, v24, v25
	v_cvt_pkrtz_f16_f32 v35, v26, v27
	ds_write2_b64 v4, v[32:33], v[34:35] offset0:132 offset1:198
	ds_write_b128 v9, v[152:155] offset:0
	ds_write_b128 v9, v[156:159] offset:1024
	ds_write_b128 v9, v[160:163] offset:2048
	ds_write_b128 v9, v[164:167] offset:3072
	s_add_u32 s3, s19, 1
	s_and_b32 s3, s3, 7
	s_lshl_b32 s3, s3, 10
	v_add_u32_e32 v11, s3, v10
	ds_read_b128 v[16:19], v11
	ds_read_b128 v[20:23], v11 offset:8192
	s_waitcnt lgkmcnt(0)
	s_barrier
	ds_read_b128 v[184:187], v7 offset:0
	ds_read_b128 v[200:203], v8 offset:0
	ds_read_b128 v[204:207], v8 offset:1024
	ds_read_b128 v[188:191], v7 offset:32
	ds_read_b128 v[208:211], v8 offset:2048
	ds_read_b128 v[212:215], v8 offset:3072
	ds_read_b128 v[192:195], v7 offset:64
	ds_read_b128 v[216:219], v8 offset:4096
	ds_read_b128 v[220:223], v8 offset:5120
	ds_read_b128 v[196:199], v7 offset:96
	ds_read_b128 v[224:227], v8 offset:6144
	ds_read_b128 v[228:231], v8 offset:7168
	s_add_u32 s3, s19, 2
	s_and_b32 s3, s3, 7
	s_lshl_b32 s57, s3, 10
	s_add_u32 s48, s57, s22
	s_add_u32 s49, s48, 0x2000
	s_add_u32 s50, s48, 0x4000
	s_add_u32 s51, s48, 0x6000
	s_add_u32 s52, s48, 0x8000
	s_add_u32 s53, s48, 0xa000
	s_add_u32 s54, s48, 0xc000
	s_add_u32 s55, s48, 0xe000
	s_lshl_b32 s56, s3, 15
	s_add_u32 s56, s56, s23
	buffer_load_dwordx4 v[88:91], v1, s[4:7], s48 offen nt
	buffer_load_dwordx4 v[92:95], v1, s[4:7], s49 offen nt
	buffer_load_dwordx4 v[96:99], v1, s[4:7], s50 offen nt
	buffer_load_dwordx4 v[100:103], v1, s[4:7], s51 offen nt
	buffer_load_dwordx4 v[104:107], v1, s[4:7], s52 offen nt
	buffer_load_dwordx4 v[108:111], v1, s[4:7], s53 offen nt
	buffer_load_dwordx4 v[112:115], v1, s[4:7], s54 offen nt
	buffer_load_dwordx4 v[116:119], v1, s[4:7], s55 offen nt
	buffer_load_dwordx4 v[152:155], v1, s[8:11], s56 offen
	buffer_load_dwordx4 v[156:159], v1, s[8:11], s56 offen offset:1024
	buffer_load_dwordx4 v[160:163], v1, s[8:11], s56 offen offset:2048
	buffer_load_dwordx4 v[164:167], v1, s[8:11], s56 offen offset:3072
	s_waitcnt vmcnt(12)
	v_pk_mul_f32 v[24:25], v[16:17], s[32:33] op_sel_hi:[1,0]
	v_pk_mul_f32 v[26:27], v[18:19], s[32:33] op_sel_hi:[1,0]
	v_pk_mul_f32 v[28:29], v[20:21], s[40:41] op_sel_hi:[1,0]
	v_pk_mul_f32 v[30:31], v[22:23], s[40:41] op_sel_hi:[1,0]
	v_cmp_lt_i32_e64 s[60:61], 0, v120
	v_cmp_lt_i32_e64 s[62:63], 0, v121
	v_cmp_lt_i32_e64 s[64:65], 0, v122
	v_cmp_lt_i32_e64 s[66:67], 0, v123
	v_max_f32_e32 v24, v24, v28
	v_max_f32_e32 v25, v25, v29
	v_max_f32_e32 v26, v26, v30
	v_max_f32_e32 v27, v27, v31
	v_cndmask_b32_e64 v24, 0, v24, s[60:61]
	v_cndmask_b32_e64 v25, 0, v25, s[62:63]
	v_cndmask_b32_e64 v26, 0, v26, s[64:65]
	v_cndmask_b32_e64 v27, 0, v27, s[66:67]
	v_cvt_pkrtz_f16_f32 v32, v24, v25
	v_cvt_pkrtz_f16_f32 v33, v26, v27
	s_waitcnt lgkmcnt(0)
	v_pk_mul_f32 v[24:25], v[16:17], s[32:33] op_sel:[0,1] op_sel_hi:[1,1]
	v_pk_mul_f32 v[26:27], v[18:19], s[32:33] op_sel:[0,1] op_sel_hi:[1,1]
	v_pk_mul_f32 v[28:29], v[20:21], s[40:41] op_sel:[0,1] op_sel_hi:[1,1]
	v_pk_mul_f32 v[30:31], v[22:23], s[40:41] op_sel:[0,1] op_sel_hi:[1,1]
	v_mfma_f32_32x32x16_f16 v[40:55], v[184:187], v[200:203], v[40:55]
	v_cmp_lt_i32_e64 s[60:61], 0, v124
	v_cmp_lt_i32_e64 s[62:63], 0, v125
	v_cmp_lt_i32_e64 s[64:65], 0, v126
	v_cmp_lt_i32_e64 s[66:67], 0, v127
	v_max_f32_e32 v24, v24, v28
	v_max_f32_e32 v25, v25, v29
	v_max_f32_e32 v26, v26, v30
	v_max_f32_e32 v27, v27, v31
	v_cndmask_b32_e64 v24, 0, v24, s[60:61]
	v_cndmask_b32_e64 v25, 0, v25, s[62:63]
	v_cndmask_b32_e64 v26, 0, v26, s[64:65]
	v_cndmask_b32_e64 v27, 0, v27, s[66:67]
	v_mfma_f32_32x32x16_f16 v[56:71], v[184:187], v[204:207], v[56:71]
	v_cvt_pkrtz_f16_f32 v34, v24, v25
	v_cvt_pkrtz_f16_f32 v35, v26, v27
	ds_write2_b64 v5, v[32:33], v[34:35] offset0:0 offset1:66
	v_pk_mul_f32 v[24:25], v[16:17], s[34:35] op_sel_hi:[1,0]
	v_pk_mul_f32 v[26:27], v[18:19], s[34:35] op_sel_hi:[1,0]
	v_pk_mul_f32 v[28:29], v[20:21], s[42:43] op_sel_hi:[1,0]
	v_pk_mul_f32 v[30:31], v[22:23], s[42:43] op_sel_hi:[1,0]
	v_mfma_f32_32x32x16_f16 v[72:87], v[184:187], v[12:15], v[72:87]
	v_cmp_lt_i32_e64 s[60:61], 0, v128
	v_cmp_lt_i32_e64 s[62:63], 0, v129
	v_cmp_lt_i32_e64 s[64:65], 0, v130
	v_cmp_lt_i32_e64 s[66:67], 0, v131
	v_max_f32_e32 v24, v24, v28
	v_max_f32_e32 v25, v25, v29
	v_max_f32_e32 v26, v26, v30
	v_max_f32_e32 v27, v27, v31
	v_cndmask_b32_e64 v24, 0, v24, s[60:61]
	v_cndmask_b32_e64 v25, 0, v25, s[62:63]
	v_cndmask_b32_e64 v26, 0, v26, s[64:65]
	v_cndmask_b32_e64 v27, 0, v27, s[66:67]
	v_mfma_f32_32x32x16_f16 v[40:55], v[188:191], v[208:211], v[40:55]
	v_cvt_pkrtz_f16_f32 v32, v24, v25
	v_cvt_pkrtz_f16_f32 v33, v26, v27
	v_pk_mul_f32 v[24:25], v[16:17], s[34:35] op_sel:[0,1] op_sel_hi:[1,1]
	v_pk_mul_f32 v[26:27], v[18:19], s[34:35] op_sel:[0,1] op_sel_hi:[1,1]
	v_pk_mul_f32 v[28:29], v[20:21], s[42:43] op_sel:[0,1] op_sel_hi:[1,1]
	v_pk_mul_f32 v[30:31], v[22:23], s[42:43] op_sel:[0,1] op_sel_hi:[1,1]
	v_mfma_f32_32x32x16_f16 v[56:71], v[188:191], v[212:215], v[56:71]
	v_cmp_lt_i32_e64 s[60:61], 0, v132
	v_cmp_lt_i32_e64 s[62:63], 0, v133
	v_cmp_lt_i32_e64 s[64:65], 0, v134
	v_cmp_lt_i32_e64 s[66:67], 0, v135
	v_max_f32_e32 v24, v24, v28
	v_max_f32_e32 v25, v25, v29
	v_max_f32_e32 v26, v26, v30
	v_max_f32_e32 v27, v27, v31
	v_cndmask_b32_e64 v24, 0, v24, s[60:61]
	v_cndmask_b32_e64 v25, 0, v25, s[62:63]
	v_cndmask_b32_e64 v26, 0, v26, s[64:65]
	v_cndmask_b32_e64 v27, 0, v27, s[66:67]
	v_mfma_f32_32x32x16_f16 v[72:87], v[188:191], v[12:15], v[72:87]
	v_cvt_pkrtz_f16_f32 v34, v24, v25
	v_cvt_pkrtz_f16_f32 v35, v26, v27
	ds_write2_b64 v5, v[32:33], v[34:35] offset0:132 offset1:198
	v_pk_mul_f32 v[24:25], v[16:17], s[36:37] op_sel_hi:[1,0]
	v_pk_mul_f32 v[26:27], v[18:19], s[36:37] op_sel_hi:[1,0]
	v_pk_mul_f32 v[28:29], v[20:21], s[44:45] op_sel_hi:[1,0]
	v_pk_mul_f32 v[30:31], v[22:23], s[44:45] op_sel_hi:[1,0]
	v_mfma_f32_32x32x16_f16 v[40:55], v[192:195], v[216:219], v[40:55]
	v_cmp_lt_i32_e64 s[60:61], 0, v136
	v_cmp_lt_i32_e64 s[62:63], 0, v137
	v_cmp_lt_i32_e64 s[64:65], 0, v138
	v_cmp_lt_i32_e64 s[66:67], 0, v139
	v_max_f32_e32 v24, v24, v28
	v_max_f32_e32 v25, v25, v29
	v_max_f32_e32 v26, v26, v30
	v_max_f32_e32 v27, v27, v31
	v_cndmask_b32_e64 v24, 0, v24, s[60:61]
	v_cndmask_b32_e64 v25, 0, v25, s[62:63]
	v_cndmask_b32_e64 v26, 0, v26, s[64:65]
	v_cndmask_b32_e64 v27, 0, v27, s[66:67]
	v_mfma_f32_32x32x16_f16 v[56:71], v[192:195], v[220:223], v[56:71]
	v_cvt_pkrtz_f16_f32 v32, v24, v25
	v_cvt_pkrtz_f16_f32 v33, v26, v27
	v_pk_mul_f32 v[24:25], v[16:17], s[36:37] op_sel:[0,1] op_sel_hi:[1,1]
	v_pk_mul_f32 v[26:27], v[18:19], s[36:37] op_sel:[0,1] op_sel_hi:[1,1]
	v_pk_mul_f32 v[28:29], v[20:21], s[44:45] op_sel:[0,1] op_sel_hi:[1,1]
	v_pk_mul_f32 v[30:31], v[22:23], s[44:45] op_sel:[0,1] op_sel_hi:[1,1]
	v_mfma_f32_32x32x16_f16 v[72:87], v[192:195], v[12:15], v[72:87]
	v_cmp_lt_i32_e64 s[60:61], 0, v140
	v_cmp_lt_i32_e64 s[62:63], 0, v141
	v_cmp_lt_i32_e64 s[64:65], 0, v142
	v_cmp_lt_i32_e64 s[66:67], 0, v143
	v_max_f32_e32 v24, v24, v28
	v_max_f32_e32 v25, v25, v29
	v_max_f32_e32 v26, v26, v30
	v_max_f32_e32 v27, v27, v31
	v_cndmask_b32_e64 v24, 0, v24, s[60:61]
	v_cndmask_b32_e64 v25, 0, v25, s[62:63]
	v_cndmask_b32_e64 v26, 0, v26, s[64:65]
	v_cndmask_b32_e64 v27, 0, v27, s[66:67]
	v_mfma_f32_32x32x16_f16 v[40:55], v[196:199], v[224:227], v[40:55]
	v_cvt_pkrtz_f16_f32 v34, v24, v25
	v_cvt_pkrtz_f16_f32 v35, v26, v27
	ds_write2_b64 v6, v[32:33], v[34:35] offset0:0 offset1:66
	v_pk_mul_f32 v[24:25], v[16:17], s[38:39] op_sel_hi:[1,0]
	v_pk_mul_f32 v[26:27], v[18:19], s[38:39] op_sel_hi:[1,0]
	v_pk_mul_f32 v[28:29], v[20:21], s[46:47] op_sel_hi:[1,0]
	v_pk_mul_f32 v[30:31], v[22:23], s[46:47] op_sel_hi:[1,0]
	v_mfma_f32_32x32x16_f16 v[56:71], v[196:199], v[228:231], v[56:71]
	v_cmp_lt_i32_e64 s[60:61], 0, v144
	v_cmp_lt_i32_e64 s[62:63], 0, v145
	v_cmp_lt_i32_e64 s[64:65], 0, v146
	v_cmp_lt_i32_e64 s[66:67], 0, v147
	v_max_f32_e32 v24, v24, v28
	v_max_f32_e32 v25, v25, v29
	v_max_f32_e32 v26, v26, v30
	v_max_f32_e32 v27, v27, v31
	v_cndmask_b32_e64 v24, 0, v24, s[60:61]
	v_cndmask_b32_e64 v25, 0, v25, s[62:63]
	v_cndmask_b32_e64 v26, 0, v26, s[64:65]
	v_cndmask_b32_e64 v27, 0, v27, s[66:67]
	v_cvt_pkrtz_f16_f32 v32, v24, v25
	v_cvt_pkrtz_f16_f32 v33, v26, v27
	v_pk_mul_f32 v[24:25], v[16:17], s[38:39] op_sel:[0,1] op_sel_hi:[1,1]
	v_pk_mul_f32 v[26:27], v[18:19], s[38:39] op_sel:[0,1] op_sel_hi:[1,1]
	v_pk_mul_f32 v[28:29], v[20:21], s[46:47] op_sel:[0,1] op_sel_hi:[1,1]
	v_pk_mul_f32 v[30:31], v[22:23], s[46:47] op_sel:[0,1] op_sel_hi:[1,1]
	v_mfma_f32_32x32x16_f16 v[72:87], v[196:199], v[12:15], v[72:87]
	v_cmp_lt_i32_e64 s[60:61], 0, v148
	v_cmp_lt_i32_e64 s[62:63], 0, v149
	v_cmp_lt_i32_e64 s[64:65], 0, v150
	v_cmp_lt_i32_e64 s[66:67], 0, v151
	v_max_f32_e32 v24, v24, v28
	v_max_f32_e32 v25, v25, v29
	v_max_f32_e32 v26, v26, v30
	v_max_f32_e32 v27, v27, v31
	v_cndmask_b32_e64 v24, 0, v24, s[60:61]
	v_cndmask_b32_e64 v25, 0, v25, s[62:63]
	v_cndmask_b32_e64 v26, 0, v26, s[64:65]
	v_cndmask_b32_e64 v27, 0, v27, s[66:67]
	v_cvt_pkrtz_f16_f32 v34, v24, v25
	v_cvt_pkrtz_f16_f32 v35, v26, v27
	ds_write2_b64 v6, v[32:33], v[34:35] offset0:132 offset1:198
	ds_write_b128 v9, v[168:171] offset:32768
	ds_write_b128 v9, v[172:175] offset:33792
	ds_write_b128 v9, v[176:179] offset:34816
	ds_write_b128 v9, v[180:183] offset:35840
	s_add_u32 s3, s19, 2
	s_and_b32 s3, s3, 7
	s_lshl_b32 s3, s3, 10
	v_add_u32_e32 v11, s3, v10
	ds_read_b128 v[16:19], v11
	ds_read_b128 v[20:23], v11 offset:8192
	s_waitcnt lgkmcnt(0)
	s_barrier
	ds_read_b128 v[184:187], v7 offset:33792
	ds_read_b128 v[200:203], v8 offset:32768
	ds_read_b128 v[204:207], v8 offset:33792
	ds_read_b128 v[188:191], v7 offset:33824
	ds_read_b128 v[208:211], v8 offset:34816
	ds_read_b128 v[212:215], v8 offset:35840
	ds_read_b128 v[192:195], v7 offset:33856
	ds_read_b128 v[216:219], v8 offset:36864
	ds_read_b128 v[220:223], v8 offset:37888
	ds_read_b128 v[196:199], v7 offset:33888
	ds_read_b128 v[224:227], v8 offset:38912
	ds_read_b128 v[228:231], v8 offset:39936
	s_add_u32 s3, s19, 3
	s_and_b32 s3, s3, 7
	s_lshl_b32 s57, s3, 10
	s_add_u32 s48, s57, s22
	s_add_u32 s49, s48, 0x2000
	s_add_u32 s50, s48, 0x4000
	s_add_u32 s51, s48, 0x6000
	s_add_u32 s52, s48, 0x8000
	s_add_u32 s53, s48, 0xa000
	s_add_u32 s54, s48, 0xc000
	s_add_u32 s55, s48, 0xe000
	s_lshl_b32 s56, s3, 15
	s_add_u32 s56, s56, s23
	buffer_load_dwordx4 v[120:123], v1, s[4:7], s48 offen nt
	buffer_load_dwordx4 v[124:127], v1, s[4:7], s49 offen nt
	buffer_load_dwordx4 v[128:131], v1, s[4:7], s50 offen nt
	buffer_load_dwordx4 v[132:135], v1, s[4:7], s51 offen nt
	buffer_load_dwordx4 v[136:139], v1, s[4:7], s52 offen nt
	buffer_load_dwordx4 v[140:143], v1, s[4:7], s53 offen nt
	buffer_load_dwordx4 v[144:147], v1, s[4:7], s54 offen nt
	buffer_load_dwordx4 v[148:151], v1, s[4:7], s55 offen nt
	buffer_load_dwordx4 v[168:171], v1, s[8:11], s56 offen
	buffer_load_dwordx4 v[172:175], v1, s[8:11], s56 offen offset:1024
	buffer_load_dwordx4 v[176:179], v1, s[8:11], s56 offen offset:2048
	buffer_load_dwordx4 v[180:183], v1, s[8:11], s56 offen offset:3072
	s_waitcnt vmcnt(12)
	v_pk_mul_f32 v[24:25], v[16:17], s[32:33] op_sel_hi:[1,0]
	v_pk_mul_f32 v[26:27], v[18:19], s[32:33] op_sel_hi:[1,0]
	v_pk_mul_f32 v[28:29], v[20:21], s[40:41] op_sel_hi:[1,0]
	v_pk_mul_f32 v[30:31], v[22:23], s[40:41] op_sel_hi:[1,0]
	v_cmp_lt_i32_e64 s[60:61], 0, v88
	v_cmp_lt_i32_e64 s[62:63], 0, v89
	v_cmp_lt_i32_e64 s[64:65], 0, v90
	v_cmp_lt_i32_e64 s[66:67], 0, v91
	v_max_f32_e32 v24, v24, v28
	v_max_f32_e32 v25, v25, v29
	v_max_f32_e32 v26, v26, v30
	v_max_f32_e32 v27, v27, v31
	v_cndmask_b32_e64 v24, 0, v24, s[60:61]
	v_cndmask_b32_e64 v25, 0, v25, s[62:63]
	v_cndmask_b32_e64 v26, 0, v26, s[64:65]
	v_cndmask_b32_e64 v27, 0, v27, s[66:67]
	v_cvt_pkrtz_f16_f32 v32, v24, v25
	v_cvt_pkrtz_f16_f32 v33, v26, v27
	s_waitcnt lgkmcnt(0)
	v_pk_mul_f32 v[24:25], v[16:17], s[32:33] op_sel:[0,1] op_sel_hi:[1,1]
	v_pk_mul_f32 v[26:27], v[18:19], s[32:33] op_sel:[0,1] op_sel_hi:[1,1]
	v_pk_mul_f32 v[28:29], v[20:21], s[40:41] op_sel:[0,1] op_sel_hi:[1,1]
	v_pk_mul_f32 v[30:31], v[22:23], s[40:41] op_sel:[0,1] op_sel_hi:[1,1]
	v_mfma_f32_32x32x16_f16 v[40:55], v[184:187], v[200:203], v[40:55]
	v_cmp_lt_i32_e64 s[60:61], 0, v92
	v_cmp_lt_i32_e64 s[62:63], 0, v93
	v_cmp_lt_i32_e64 s[64:65], 0, v94
	v_cmp_lt_i32_e64 s[66:67], 0, v95
	v_max_f32_e32 v24, v24, v28
	v_max_f32_e32 v25, v25, v29
	v_max_f32_e32 v26, v26, v30
	v_max_f32_e32 v27, v27, v31
	v_cndmask_b32_e64 v24, 0, v24, s[60:61]
	v_cndmask_b32_e64 v25, 0, v25, s[62:63]
	v_cndmask_b32_e64 v26, 0, v26, s[64:65]
	v_cndmask_b32_e64 v27, 0, v27, s[66:67]
	v_mfma_f32_32x32x16_f16 v[56:71], v[184:187], v[204:207], v[56:71]
	v_cvt_pkrtz_f16_f32 v34, v24, v25
	v_cvt_pkrtz_f16_f32 v35, v26, v27
	ds_write2_b64 v3, v[32:33], v[34:35] offset0:0 offset1:66
	v_pk_mul_f32 v[24:25], v[16:17], s[34:35] op_sel_hi:[1,0]
	v_pk_mul_f32 v[26:27], v[18:19], s[34:35] op_sel_hi:[1,0]
	v_pk_mul_f32 v[28:29], v[20:21], s[42:43] op_sel_hi:[1,0]
	v_pk_mul_f32 v[30:31], v[22:23], s[42:43] op_sel_hi:[1,0]
	v_mfma_f32_32x32x16_f16 v[72:87], v[184:187], v[12:15], v[72:87]
	v_cmp_lt_i32_e64 s[60:61], 0, v96
	v_cmp_lt_i32_e64 s[62:63], 0, v97
	v_cmp_lt_i32_e64 s[64:65], 0, v98
	v_cmp_lt_i32_e64 s[66:67], 0, v99
	v_max_f32_e32 v24, v24, v28
	v_max_f32_e32 v25, v25, v29
	v_max_f32_e32 v26, v26, v30
	v_max_f32_e32 v27, v27, v31
	v_cndmask_b32_e64 v24, 0, v24, s[60:61]
	v_cndmask_b32_e64 v25, 0, v25, s[62:63]
	v_cndmask_b32_e64 v26, 0, v26, s[64:65]
	v_cndmask_b32_e64 v27, 0, v27, s[66:67]
	v_mfma_f32_32x32x16_f16 v[40:55], v[188:191], v[208:211], v[40:55]
	v_cvt_pkrtz_f16_f32 v32, v24, v25
	v_cvt_pkrtz_f16_f32 v33, v26, v27
	v_pk_mul_f32 v[24:25], v[16:17], s[34:35] op_sel:[0,1] op_sel_hi:[1,1]
	v_pk_mul_f32 v[26:27], v[18:19], s[34:35] op_sel:[0,1] op_sel_hi:[1,1]
	v_pk_mul_f32 v[28:29], v[20:21], s[42:43] op_sel:[0,1] op_sel_hi:[1,1]
	v_pk_mul_f32 v[30:31], v[22:23], s[42:43] op_sel:[0,1] op_sel_hi:[1,1]
	v_mfma_f32_32x32x16_f16 v[56:71], v[188:191], v[212:215], v[56:71]
	v_cmp_lt_i32_e64 s[60:61], 0, v100
	v_cmp_lt_i32_e64 s[62:63], 0, v101
	v_cmp_lt_i32_e64 s[64:65], 0, v102
	v_cmp_lt_i32_e64 s[66:67], 0, v103
	v_max_f32_e32 v24, v24, v28
	v_max_f32_e32 v25, v25, v29
	v_max_f32_e32 v26, v26, v30
	v_max_f32_e32 v27, v27, v31
	v_cndmask_b32_e64 v24, 0, v24, s[60:61]
	v_cndmask_b32_e64 v25, 0, v25, s[62:63]
	v_cndmask_b32_e64 v26, 0, v26, s[64:65]
	v_cndmask_b32_e64 v27, 0, v27, s[66:67]
	v_mfma_f32_32x32x16_f16 v[72:87], v[188:191], v[12:15], v[72:87]
	v_cvt_pkrtz_f16_f32 v34, v24, v25
	v_cvt_pkrtz_f16_f32 v35, v26, v27
	ds_write2_b64 v3, v[32:33], v[34:35] offset0:132 offset1:198
	v_pk_mul_f32 v[24:25], v[16:17], s[36:37] op_sel_hi:[1,0]
	v_pk_mul_f32 v[26:27], v[18:19], s[36:37] op_sel_hi:[1,0]
	v_pk_mul_f32 v[28:29], v[20:21], s[44:45] op_sel_hi:[1,0]
	v_pk_mul_f32 v[30:31], v[22:23], s[44:45] op_sel_hi:[1,0]
	v_mfma_f32_32x32x16_f16 v[40:55], v[192:195], v[216:219], v[40:55]
	v_cmp_lt_i32_e64 s[60:61], 0, v104
	v_cmp_lt_i32_e64 s[62:63], 0, v105
	v_cmp_lt_i32_e64 s[64:65], 0, v106
	v_cmp_lt_i32_e64 s[66:67], 0, v107
	v_max_f32_e32 v24, v24, v28
	v_max_f32_e32 v25, v25, v29
	v_max_f32_e32 v26, v26, v30
	v_max_f32_e32 v27, v27, v31
	v_cndmask_b32_e64 v24, 0, v24, s[60:61]
	v_cndmask_b32_e64 v25, 0, v25, s[62:63]
	v_cndmask_b32_e64 v26, 0, v26, s[64:65]
	v_cndmask_b32_e64 v27, 0, v27, s[66:67]
	v_mfma_f32_32x32x16_f16 v[56:71], v[192:195], v[220:223], v[56:71]
	v_cvt_pkrtz_f16_f32 v32, v24, v25
	v_cvt_pkrtz_f16_f32 v33, v26, v27
	v_pk_mul_f32 v[24:25], v[16:17], s[36:37] op_sel:[0,1] op_sel_hi:[1,1]
	v_pk_mul_f32 v[26:27], v[18:19], s[36:37] op_sel:[0,1] op_sel_hi:[1,1]
	v_pk_mul_f32 v[28:29], v[20:21], s[44:45] op_sel:[0,1] op_sel_hi:[1,1]
	v_pk_mul_f32 v[30:31], v[22:23], s[44:45] op_sel:[0,1] op_sel_hi:[1,1]
	v_mfma_f32_32x32x16_f16 v[72:87], v[192:195], v[12:15], v[72:87]
	v_cmp_lt_i32_e64 s[60:61], 0, v108
	v_cmp_lt_i32_e64 s[62:63], 0, v109
	v_cmp_lt_i32_e64 s[64:65], 0, v110
	v_cmp_lt_i32_e64 s[66:67], 0, v111
	v_max_f32_e32 v24, v24, v28
	v_max_f32_e32 v25, v25, v29
	v_max_f32_e32 v26, v26, v30
	v_max_f32_e32 v27, v27, v31
	v_cndmask_b32_e64 v24, 0, v24, s[60:61]
	v_cndmask_b32_e64 v25, 0, v25, s[62:63]
	v_cndmask_b32_e64 v26, 0, v26, s[64:65]
	v_cndmask_b32_e64 v27, 0, v27, s[66:67]
	v_mfma_f32_32x32x16_f16 v[40:55], v[196:199], v[224:227], v[40:55]
	v_cvt_pkrtz_f16_f32 v34, v24, v25
	v_cvt_pkrtz_f16_f32 v35, v26, v27
	ds_write2_b64 v4, v[32:33], v[34:35] offset0:0 offset1:66
	v_pk_mul_f32 v[24:25], v[16:17], s[38:39] op_sel_hi:[1,0]
	v_pk_mul_f32 v[26:27], v[18:19], s[38:39] op_sel_hi:[1,0]
	v_pk_mul_f32 v[28:29], v[20:21], s[46:47] op_sel_hi:[1,0]
	v_pk_mul_f32 v[30:31], v[22:23], s[46:47] op_sel_hi:[1,0]
	v_mfma_f32_32x32x16_f16 v[56:71], v[196:199], v[228:231], v[56:71]
	v_cmp_lt_i32_e64 s[60:61], 0, v112
	v_cmp_lt_i32_e64 s[62:63], 0, v113
	v_cmp_lt_i32_e64 s[64:65], 0, v114
	v_cmp_lt_i32_e64 s[66:67], 0, v115
	v_max_f32_e32 v24, v24, v28
	v_max_f32_e32 v25, v25, v29
	v_max_f32_e32 v26, v26, v30
	v_max_f32_e32 v27, v27, v31
	v_cndmask_b32_e64 v24, 0, v24, s[60:61]
	v_cndmask_b32_e64 v25, 0, v25, s[62:63]
	v_cndmask_b32_e64 v26, 0, v26, s[64:65]
	v_cndmask_b32_e64 v27, 0, v27, s[66:67]
	v_cvt_pkrtz_f16_f32 v32, v24, v25
	v_cvt_pkrtz_f16_f32 v33, v26, v27
	v_pk_mul_f32 v[24:25], v[16:17], s[38:39] op_sel:[0,1] op_sel_hi:[1,1]
	v_pk_mul_f32 v[26:27], v[18:19], s[38:39] op_sel:[0,1] op_sel_hi:[1,1]
	v_pk_mul_f32 v[28:29], v[20:21], s[46:47] op_sel:[0,1] op_sel_hi:[1,1]
	v_pk_mul_f32 v[30:31], v[22:23], s[46:47] op_sel:[0,1] op_sel_hi:[1,1]
	v_mfma_f32_32x32x16_f16 v[72:87], v[196:199], v[12:15], v[72:87]
	v_cmp_lt_i32_e64 s[60:61], 0, v116
	v_cmp_lt_i32_e64 s[62:63], 0, v117
	v_cmp_lt_i32_e64 s[64:65], 0, v118
	v_cmp_lt_i32_e64 s[66:67], 0, v119
	v_max_f32_e32 v24, v24, v28
	v_max_f32_e32 v25, v25, v29
	v_max_f32_e32 v26, v26, v30
	v_max_f32_e32 v27, v27, v31
	v_cndmask_b32_e64 v24, 0, v24, s[60:61]
	v_cndmask_b32_e64 v25, 0, v25, s[62:63]
	v_cndmask_b32_e64 v26, 0, v26, s[64:65]
	v_cndmask_b32_e64 v27, 0, v27, s[66:67]
	v_cvt_pkrtz_f16_f32 v34, v24, v25
	v_cvt_pkrtz_f16_f32 v35, v26, v27
	ds_write2_b64 v4, v[32:33], v[34:35] offset0:132 offset1:198
	ds_write_b128 v9, v[152:155] offset:0
	ds_write_b128 v9, v[156:159] offset:1024
	ds_write_b128 v9, v[160:163] offset:2048
	ds_write_b128 v9, v[164:167] offset:3072
	s_add_u32 s3, s19, 3
	s_and_b32 s3, s3, 7
	s_lshl_b32 s3, s3, 10
	v_add_u32_e32 v11, s3, v10
	ds_read_b128 v[16:19], v11
	ds_read_b128 v[20:23], v11 offset:8192
	s_waitcnt lgkmcnt(0)
	s_barrier
	ds_read_b128 v[184:187], v7 offset:0
	ds_read_b128 v[200:203], v8 offset:0
	ds_read_b128 v[204:207], v8 offset:1024
	ds_read_b128 v[188:191], v7 offset:32
	ds_read_b128 v[208:211], v8 offset:2048
	ds_read_b128 v[212:215], v8 offset:3072
	ds_read_b128 v[192:195], v7 offset:64
	ds_read_b128 v[216:219], v8 offset:4096
	ds_read_b128 v[220:223], v8 offset:5120
	ds_read_b128 v[196:199], v7 offset:96
	ds_read_b128 v[224:227], v8 offset:6144
	ds_read_b128 v[228:231], v8 offset:7168
	s_add_u32 s3, s19, 4
	s_and_b32 s3, s3, 7
	s_lshl_b32 s57, s3, 10
	s_add_u32 s48, s57, s22
	s_add_u32 s49, s48, 0x2000
	s_add_u32 s50, s48, 0x4000
	s_add_u32 s51, s48, 0x6000
	s_add_u32 s52, s48, 0x8000
	s_add_u32 s53, s48, 0xa000
	s_add_u32 s54, s48, 0xc000
	s_add_u32 s55, s48, 0xe000
	s_lshl_b32 s56, s3, 15
	s_add_u32 s56, s56, s23
	buffer_load_dwordx4 v[88:91], v1, s[4:7], s48 offen nt
	buffer_load_dwordx4 v[92:95], v1, s[4:7], s49 offen nt
	buffer_load_dwordx4 v[96:99], v1, s[4:7], s50 offen nt
	buffer_load_dwordx4 v[100:103], v1, s[4:7], s51 offen nt
	buffer_load_dwordx4 v[104:107], v1, s[4:7], s52 offen nt
	buffer_load_dwordx4 v[108:111], v1, s[4:7], s53 offen nt
	buffer_load_dwordx4 v[112:115], v1, s[4:7], s54 offen nt
	buffer_load_dwordx4 v[116:119], v1, s[4:7], s55 offen nt
	buffer_load_dwordx4 v[152:155], v1, s[8:11], s56 offen
	buffer_load_dwordx4 v[156:159], v1, s[8:11], s56 offen offset:1024
	buffer_load_dwordx4 v[160:163], v1, s[8:11], s56 offen offset:2048
	buffer_load_dwordx4 v[164:167], v1, s[8:11], s56 offen offset:3072
	s_waitcnt vmcnt(12)
	v_pk_mul_f32 v[24:25], v[16:17], s[32:33] op_sel_hi:[1,0]
	v_pk_mul_f32 v[26:27], v[18:19], s[32:33] op_sel_hi:[1,0]
	v_pk_mul_f32 v[28:29], v[20:21], s[40:41] op_sel_hi:[1,0]
	v_pk_mul_f32 v[30:31], v[22:23], s[40:41] op_sel_hi:[1,0]
	v_cmp_lt_i32_e64 s[60:61], 0, v120
	v_cmp_lt_i32_e64 s[62:63], 0, v121
	v_cmp_lt_i32_e64 s[64:65], 0, v122
	v_cmp_lt_i32_e64 s[66:67], 0, v123
	v_max_f32_e32 v24, v24, v28
	v_max_f32_e32 v25, v25, v29
	v_max_f32_e32 v26, v26, v30
	v_max_f32_e32 v27, v27, v31
	v_cndmask_b32_e64 v24, 0, v24, s[60:61]
	v_cndmask_b32_e64 v25, 0, v25, s[62:63]
	v_cndmask_b32_e64 v26, 0, v26, s[64:65]
	v_cndmask_b32_e64 v27, 0, v27, s[66:67]
	v_cvt_pkrtz_f16_f32 v32, v24, v25
	v_cvt_pkrtz_f16_f32 v33, v26, v27
	s_waitcnt lgkmcnt(0)
	v_pk_mul_f32 v[24:25], v[16:17], s[32:33] op_sel:[0,1] op_sel_hi:[1,1]
	v_pk_mul_f32 v[26:27], v[18:19], s[32:33] op_sel:[0,1] op_sel_hi:[1,1]
	v_pk_mul_f32 v[28:29], v[20:21], s[40:41] op_sel:[0,1] op_sel_hi:[1,1]
	v_pk_mul_f32 v[30:31], v[22:23], s[40:41] op_sel:[0,1] op_sel_hi:[1,1]
	v_mfma_f32_32x32x16_f16 v[40:55], v[184:187], v[200:203], v[40:55]
	v_cmp_lt_i32_e64 s[60:61], 0, v124
	v_cmp_lt_i32_e64 s[62:63], 0, v125
	v_cmp_lt_i32_e64 s[64:65], 0, v126
	v_cmp_lt_i32_e64 s[66:67], 0, v127
	v_max_f32_e32 v24, v24, v28
	v_max_f32_e32 v25, v25, v29
	v_max_f32_e32 v26, v26, v30
	v_max_f32_e32 v27, v27, v31
	v_cndmask_b32_e64 v24, 0, v24, s[60:61]
	v_cndmask_b32_e64 v25, 0, v25, s[62:63]
	v_cndmask_b32_e64 v26, 0, v26, s[64:65]
	v_cndmask_b32_e64 v27, 0, v27, s[66:67]
	v_mfma_f32_32x32x16_f16 v[56:71], v[184:187], v[204:207], v[56:71]
	v_cvt_pkrtz_f16_f32 v34, v24, v25
	v_cvt_pkrtz_f16_f32 v35, v26, v27
	ds_write2_b64 v5, v[32:33], v[34:35] offset0:0 offset1:66
	v_pk_mul_f32 v[24:25], v[16:17], s[34:35] op_sel_hi:[1,0]
	v_pk_mul_f32 v[26:27], v[18:19], s[34:35] op_sel_hi:[1,0]
	v_pk_mul_f32 v[28:29], v[20:21], s[42:43] op_sel_hi:[1,0]
	v_pk_mul_f32 v[30:31], v[22:23], s[42:43] op_sel_hi:[1,0]
	v_mfma_f32_32x32x16_f16 v[72:87], v[184:187], v[12:15], v[72:87]
	v_cmp_lt_i32_e64 s[60:61], 0, v128
	v_cmp_lt_i32_e64 s[62:63], 0, v129
	v_cmp_lt_i32_e64 s[64:65], 0, v130
	v_cmp_lt_i32_e64 s[66:67], 0, v131
	v_max_f32_e32 v24, v24, v28
	v_max_f32_e32 v25, v25, v29
	v_max_f32_e32 v26, v26, v30
	v_max_f32_e32 v27, v27, v31
	v_cndmask_b32_e64 v24, 0, v24, s[60:61]
	v_cndmask_b32_e64 v25, 0, v25, s[62:63]
	v_cndmask_b32_e64 v26, 0, v26, s[64:65]
	v_cndmask_b32_e64 v27, 0, v27, s[66:67]
	v_mfma_f32_32x32x16_f16 v[40:55], v[188:191], v[208:211], v[40:55]
	v_cvt_pkrtz_f16_f32 v32, v24, v25
	v_cvt_pkrtz_f16_f32 v33, v26, v27
	v_pk_mul_f32 v[24:25], v[16:17], s[34:35] op_sel:[0,1] op_sel_hi:[1,1]
	v_pk_mul_f32 v[26:27], v[18:19], s[34:35] op_sel:[0,1] op_sel_hi:[1,1]
	v_pk_mul_f32 v[28:29], v[20:21], s[42:43] op_sel:[0,1] op_sel_hi:[1,1]
	v_pk_mul_f32 v[30:31], v[22:23], s[42:43] op_sel:[0,1] op_sel_hi:[1,1]
	v_mfma_f32_32x32x16_f16 v[56:71], v[188:191], v[212:215], v[56:71]
	v_cmp_lt_i32_e64 s[60:61], 0, v132
	v_cmp_lt_i32_e64 s[62:63], 0, v133
	v_cmp_lt_i32_e64 s[64:65], 0, v134
	v_cmp_lt_i32_e64 s[66:67], 0, v135
	v_max_f32_e32 v24, v24, v28
	v_max_f32_e32 v25, v25, v29
	v_max_f32_e32 v26, v26, v30
	v_max_f32_e32 v27, v27, v31
	v_cndmask_b32_e64 v24, 0, v24, s[60:61]
	v_cndmask_b32_e64 v25, 0, v25, s[62:63]
	v_cndmask_b32_e64 v26, 0, v26, s[64:65]
	v_cndmask_b32_e64 v27, 0, v27, s[66:67]
	v_mfma_f32_32x32x16_f16 v[72:87], v[188:191], v[12:15], v[72:87]
	v_cvt_pkrtz_f16_f32 v34, v24, v25
	v_cvt_pkrtz_f16_f32 v35, v26, v27
	ds_write2_b64 v5, v[32:33], v[34:35] offset0:132 offset1:198
	v_pk_mul_f32 v[24:25], v[16:17], s[36:37] op_sel_hi:[1,0]
	v_pk_mul_f32 v[26:27], v[18:19], s[36:37] op_sel_hi:[1,0]
	v_pk_mul_f32 v[28:29], v[20:21], s[44:45] op_sel_hi:[1,0]
	v_pk_mul_f32 v[30:31], v[22:23], s[44:45] op_sel_hi:[1,0]
	v_mfma_f32_32x32x16_f16 v[40:55], v[192:195], v[216:219], v[40:55]
	v_cmp_lt_i32_e64 s[60:61], 0, v136
	v_cmp_lt_i32_e64 s[62:63], 0, v137
	v_cmp_lt_i32_e64 s[64:65], 0, v138
	v_cmp_lt_i32_e64 s[66:67], 0, v139
	v_max_f32_e32 v24, v24, v28
	v_max_f32_e32 v25, v25, v29
	v_max_f32_e32 v26, v26, v30
	v_max_f32_e32 v27, v27, v31
	v_cndmask_b32_e64 v24, 0, v24, s[60:61]
	v_cndmask_b32_e64 v25, 0, v25, s[62:63]
	v_cndmask_b32_e64 v26, 0, v26, s[64:65]
	v_cndmask_b32_e64 v27, 0, v27, s[66:67]
	v_mfma_f32_32x32x16_f16 v[56:71], v[192:195], v[220:223], v[56:71]
	v_cvt_pkrtz_f16_f32 v32, v24, v25
	v_cvt_pkrtz_f16_f32 v33, v26, v27
	v_pk_mul_f32 v[24:25], v[16:17], s[36:37] op_sel:[0,1] op_sel_hi:[1,1]
	v_pk_mul_f32 v[26:27], v[18:19], s[36:37] op_sel:[0,1] op_sel_hi:[1,1]
	v_pk_mul_f32 v[28:29], v[20:21], s[44:45] op_sel:[0,1] op_sel_hi:[1,1]
	v_pk_mul_f32 v[30:31], v[22:23], s[44:45] op_sel:[0,1] op_sel_hi:[1,1]
	v_mfma_f32_32x32x16_f16 v[72:87], v[192:195], v[12:15], v[72:87]
	v_cmp_lt_i32_e64 s[60:61], 0, v140
	v_cmp_lt_i32_e64 s[62:63], 0, v141
	v_cmp_lt_i32_e64 s[64:65], 0, v142
	v_cmp_lt_i32_e64 s[66:67], 0, v143
	v_max_f32_e32 v24, v24, v28
	v_max_f32_e32 v25, v25, v29
	v_max_f32_e32 v26, v26, v30
	v_max_f32_e32 v27, v27, v31
	v_cndmask_b32_e64 v24, 0, v24, s[60:61]
	v_cndmask_b32_e64 v25, 0, v25, s[62:63]
	v_cndmask_b32_e64 v26, 0, v26, s[64:65]
	v_cndmask_b32_e64 v27, 0, v27, s[66:67]
	v_mfma_f32_32x32x16_f16 v[40:55], v[196:199], v[224:227], v[40:55]
	v_cvt_pkrtz_f16_f32 v34, v24, v25
	v_cvt_pkrtz_f16_f32 v35, v26, v27
	ds_write2_b64 v6, v[32:33], v[34:35] offset0:0 offset1:66
	v_pk_mul_f32 v[24:25], v[16:17], s[38:39] op_sel_hi:[1,0]
	v_pk_mul_f32 v[26:27], v[18:19], s[38:39] op_sel_hi:[1,0]
	v_pk_mul_f32 v[28:29], v[20:21], s[46:47] op_sel_hi:[1,0]
	v_pk_mul_f32 v[30:31], v[22:23], s[46:47] op_sel_hi:[1,0]
	v_mfma_f32_32x32x16_f16 v[56:71], v[196:199], v[228:231], v[56:71]
	v_cmp_lt_i32_e64 s[60:61], 0, v144
	v_cmp_lt_i32_e64 s[62:63], 0, v145
	v_cmp_lt_i32_e64 s[64:65], 0, v146
	v_cmp_lt_i32_e64 s[66:67], 0, v147
	v_max_f32_e32 v24, v24, v28
	v_max_f32_e32 v25, v25, v29
	v_max_f32_e32 v26, v26, v30
	v_max_f32_e32 v27, v27, v31
	v_cndmask_b32_e64 v24, 0, v24, s[60:61]
	v_cndmask_b32_e64 v25, 0, v25, s[62:63]
	v_cndmask_b32_e64 v26, 0, v26, s[64:65]
	v_cndmask_b32_e64 v27, 0, v27, s[66:67]
	v_cvt_pkrtz_f16_f32 v32, v24, v25
	v_cvt_pkrtz_f16_f32 v33, v26, v27
	v_pk_mul_f32 v[24:25], v[16:17], s[38:39] op_sel:[0,1] op_sel_hi:[1,1]
	v_pk_mul_f32 v[26:27], v[18:19], s[38:39] op_sel:[0,1] op_sel_hi:[1,1]
	v_pk_mul_f32 v[28:29], v[20:21], s[46:47] op_sel:[0,1] op_sel_hi:[1,1]
	v_pk_mul_f32 v[30:31], v[22:23], s[46:47] op_sel:[0,1] op_sel_hi:[1,1]
	v_mfma_f32_32x32x16_f16 v[72:87], v[196:199], v[12:15], v[72:87]
	v_cmp_lt_i32_e64 s[60:61], 0, v148
	v_cmp_lt_i32_e64 s[62:63], 0, v149
	v_cmp_lt_i32_e64 s[64:65], 0, v150
	v_cmp_lt_i32_e64 s[66:67], 0, v151
	v_max_f32_e32 v24, v24, v28
	v_max_f32_e32 v25, v25, v29
	v_max_f32_e32 v26, v26, v30
	v_max_f32_e32 v27, v27, v31
	v_cndmask_b32_e64 v24, 0, v24, s[60:61]
	v_cndmask_b32_e64 v25, 0, v25, s[62:63]
	v_cndmask_b32_e64 v26, 0, v26, s[64:65]
	v_cndmask_b32_e64 v27, 0, v27, s[66:67]
	v_cvt_pkrtz_f16_f32 v34, v24, v25
	v_cvt_pkrtz_f16_f32 v35, v26, v27
	ds_write2_b64 v6, v[32:33], v[34:35] offset0:132 offset1:198
	ds_write_b128 v9, v[168:171] offset:32768
	ds_write_b128 v9, v[172:175] offset:33792
	ds_write_b128 v9, v[176:179] offset:34816
	ds_write_b128 v9, v[180:183] offset:35840
	s_add_u32 s3, s19, 4
	s_and_b32 s3, s3, 7
	s_lshl_b32 s3, s3, 10
	v_add_u32_e32 v11, s3, v10
	ds_read_b128 v[16:19], v11
	ds_read_b128 v[20:23], v11 offset:8192
	s_waitcnt lgkmcnt(0)
	s_barrier
	ds_read_b128 v[184:187], v7 offset:33792
	ds_read_b128 v[200:203], v8 offset:32768
	ds_read_b128 v[204:207], v8 offset:33792
	ds_read_b128 v[188:191], v7 offset:33824
	ds_read_b128 v[208:211], v8 offset:34816
	ds_read_b128 v[212:215], v8 offset:35840
	ds_read_b128 v[192:195], v7 offset:33856
	ds_read_b128 v[216:219], v8 offset:36864
	ds_read_b128 v[220:223], v8 offset:37888
	ds_read_b128 v[196:199], v7 offset:33888
	ds_read_b128 v[224:227], v8 offset:38912
	ds_read_b128 v[228:231], v8 offset:39936
	s_add_u32 s3, s19, 5
	s_and_b32 s3, s3, 7
	s_lshl_b32 s57, s3, 10
	s_add_u32 s48, s57, s22
	s_add_u32 s49, s48, 0x2000
	s_add_u32 s50, s48, 0x4000
	s_add_u32 s51, s48, 0x6000
	s_add_u32 s52, s48, 0x8000
	s_add_u32 s53, s48, 0xa000
	s_add_u32 s54, s48, 0xc000
	s_add_u32 s55, s48, 0xe000
	s_lshl_b32 s56, s3, 15
	s_add_u32 s56, s56, s23
	buffer_load_dwordx4 v[120:123], v1, s[4:7], s48 offen nt
	buffer_load_dwordx4 v[124:127], v1, s[4:7], s49 offen nt
	buffer_load_dwordx4 v[128:131], v1, s[4:7], s50 offen nt
	buffer_load_dwordx4 v[132:135], v1, s[4:7], s51 offen nt
	buffer_load_dwordx4 v[136:139], v1, s[4:7], s52 offen nt
	buffer_load_dwordx4 v[140:143], v1, s[4:7], s53 offen nt
	buffer_load_dwordx4 v[144:147], v1, s[4:7], s54 offen nt
	buffer_load_dwordx4 v[148:151], v1, s[4:7], s55 offen nt
	buffer_load_dwordx4 v[168:171], v1, s[8:11], s56 offen
	buffer_load_dwordx4 v[172:175], v1, s[8:11], s56 offen offset:1024
	buffer_load_dwordx4 v[176:179], v1, s[8:11], s56 offen offset:2048
	buffer_load_dwordx4 v[180:183], v1, s[8:11], s56 offen offset:3072
	s_waitcnt vmcnt(12)
	v_pk_mul_f32 v[24:25], v[16:17], s[32:33] op_sel_hi:[1,0]
	v_pk_mul_f32 v[26:27], v[18:19], s[32:33] op_sel_hi:[1,0]
	v_pk_mul_f32 v[28:29], v[20:21], s[40:41] op_sel_hi:[1,0]
	v_pk_mul_f32 v[30:31], v[22:23], s[40:41] op_sel_hi:[1,0]
	v_cmp_lt_i32_e64 s[60:61], 0, v88
	v_cmp_lt_i32_e64 s[62:63], 0, v89
	v_cmp_lt_i32_e64 s[64:65], 0, v90
	v_cmp_lt_i32_e64 s[66:67], 0, v91
	v_max_f32_e32 v24, v24, v28
	v_max_f32_e32 v25, v25, v29
	v_max_f32_e32 v26, v26, v30
	v_max_f32_e32 v27, v27, v31
	v_cndmask_b32_e64 v24, 0, v24, s[60:61]
	v_cndmask_b32_e64 v25, 0, v25, s[62:63]
	v_cndmask_b32_e64 v26, 0, v26, s[64:65]
	v_cndmask_b32_e64 v27, 0, v27, s[66:67]
	v_cvt_pkrtz_f16_f32 v32, v24, v25
	v_cvt_pkrtz_f16_f32 v33, v26, v27
	s_waitcnt lgkmcnt(0)
	v_pk_mul_f32 v[24:25], v[16:17], s[32:33] op_sel:[0,1] op_sel_hi:[1,1]
	v_pk_mul_f32 v[26:27], v[18:19], s[32:33] op_sel:[0,1] op_sel_hi:[1,1]
	v_pk_mul_f32 v[28:29], v[20:21], s[40:41] op_sel:[0,1] op_sel_hi:[1,1]
	v_pk_mul_f32 v[30:31], v[22:23], s[40:41] op_sel:[0,1] op_sel_hi:[1,1]
	v_mfma_f32_32x32x16_f16 v[40:55], v[184:187], v[200:203], v[40:55]
	v_cmp_lt_i32_e64 s[60:61], 0, v92
	v_cmp_lt_i32_e64 s[62:63], 0, v93
	v_cmp_lt_i32_e64 s[64:65], 0, v94
	v_cmp_lt_i32_e64 s[66:67], 0, v95
	v_max_f32_e32 v24, v24, v28
	v_max_f32_e32 v25, v25, v29
	v_max_f32_e32 v26, v26, v30
	v_max_f32_e32 v27, v27, v31
	v_cndmask_b32_e64 v24, 0, v24, s[60:61]
	v_cndmask_b32_e64 v25, 0, v25, s[62:63]
	v_cndmask_b32_e64 v26, 0, v26, s[64:65]
	v_cndmask_b32_e64 v27, 0, v27, s[66:67]
	v_mfma_f32_32x32x16_f16 v[56:71], v[184:187], v[204:207], v[56:71]
	v_cvt_pkrtz_f16_f32 v34, v24, v25
	v_cvt_pkrtz_f16_f32 v35, v26, v27
	ds_write2_b64 v3, v[32:33], v[34:35] offset0:0 offset1:66
	v_pk_mul_f32 v[24:25], v[16:17], s[34:35] op_sel_hi:[1,0]
	v_pk_mul_f32 v[26:27], v[18:19], s[34:35] op_sel_hi:[1,0]
	v_pk_mul_f32 v[28:29], v[20:21], s[42:43] op_sel_hi:[1,0]
	v_pk_mul_f32 v[30:31], v[22:23], s[42:43] op_sel_hi:[1,0]
	v_mfma_f32_32x32x16_f16 v[72:87], v[184:187], v[12:15], v[72:87]
	v_cmp_lt_i32_e64 s[60:61], 0, v96
	v_cmp_lt_i32_e64 s[62:63], 0, v97
	v_cmp_lt_i32_e64 s[64:65], 0, v98
	v_cmp_lt_i32_e64 s[66:67], 0, v99
	v_max_f32_e32 v24, v24, v28
	v_max_f32_e32 v25, v25, v29
	v_max_f32_e32 v26, v26, v30
	v_max_f32_e32 v27, v27, v31
	v_cndmask_b32_e64 v24, 0, v24, s[60:61]
	v_cndmask_b32_e64 v25, 0, v25, s[62:63]
	v_cndmask_b32_e64 v26, 0, v26, s[64:65]
	v_cndmask_b32_e64 v27, 0, v27, s[66:67]
	v_mfma_f32_32x32x16_f16 v[40:55], v[188:191], v[208:211], v[40:55]
	v_cvt_pkrtz_f16_f32 v32, v24, v25
	v_cvt_pkrtz_f16_f32 v33, v26, v27
	v_pk_mul_f32 v[24:25], v[16:17], s[34:35] op_sel:[0,1] op_sel_hi:[1,1]
	v_pk_mul_f32 v[26:27], v[18:19], s[34:35] op_sel:[0,1] op_sel_hi:[1,1]
	v_pk_mul_f32 v[28:29], v[20:21], s[42:43] op_sel:[0,1] op_sel_hi:[1,1]
	v_pk_mul_f32 v[30:31], v[22:23], s[42:43] op_sel:[0,1] op_sel_hi:[1,1]
	v_mfma_f32_32x32x16_f16 v[56:71], v[188:191], v[212:215], v[56:71]
	v_cmp_lt_i32_e64 s[60:61], 0, v100
	v_cmp_lt_i32_e64 s[62:63], 0, v101
	v_cmp_lt_i32_e64 s[64:65], 0, v102
	v_cmp_lt_i32_e64 s[66:67], 0, v103
	v_max_f32_e32 v24, v24, v28
	v_max_f32_e32 v25, v25, v29
	v_max_f32_e32 v26, v26, v30
	v_max_f32_e32 v27, v27, v31
	v_cndmask_b32_e64 v24, 0, v24, s[60:61]
	v_cndmask_b32_e64 v25, 0, v25, s[62:63]
	v_cndmask_b32_e64 v26, 0, v26, s[64:65]
	v_cndmask_b32_e64 v27, 0, v27, s[66:67]
	v_mfma_f32_32x32x16_f16 v[72:87], v[188:191], v[12:15], v[72:87]
	v_cvt_pkrtz_f16_f32 v34, v24, v25
	v_cvt_pkrtz_f16_f32 v35, v26, v27
	ds_write2_b64 v3, v[32:33], v[34:35] offset0:132 offset1:198
	v_pk_mul_f32 v[24:25], v[16:17], s[36:37] op_sel_hi:[1,0]
	v_pk_mul_f32 v[26:27], v[18:19], s[36:37] op_sel_hi:[1,0]
	v_pk_mul_f32 v[28:29], v[20:21], s[44:45] op_sel_hi:[1,0]
	v_pk_mul_f32 v[30:31], v[22:23], s[44:45] op_sel_hi:[1,0]
	v_mfma_f32_32x32x16_f16 v[40:55], v[192:195], v[216:219], v[40:55]
	v_cmp_lt_i32_e64 s[60:61], 0, v104
	v_cmp_lt_i32_e64 s[62:63], 0, v105
	v_cmp_lt_i32_e64 s[64:65], 0, v106
	v_cmp_lt_i32_e64 s[66:67], 0, v107
	v_max_f32_e32 v24, v24, v28
	v_max_f32_e32 v25, v25, v29
	v_max_f32_e32 v26, v26, v30
	v_max_f32_e32 v27, v27, v31
	v_cndmask_b32_e64 v24, 0, v24, s[60:61]
	v_cndmask_b32_e64 v25, 0, v25, s[62:63]
	v_cndmask_b32_e64 v26, 0, v26, s[64:65]
	v_cndmask_b32_e64 v27, 0, v27, s[66:67]
	v_mfma_f32_32x32x16_f16 v[56:71], v[192:195], v[220:223], v[56:71]
	v_cvt_pkrtz_f16_f32 v32, v24, v25
	v_cvt_pkrtz_f16_f32 v33, v26, v27
	v_pk_mul_f32 v[24:25], v[16:17], s[36:37] op_sel:[0,1] op_sel_hi:[1,1]
	v_pk_mul_f32 v[26:27], v[18:19], s[36:37] op_sel:[0,1] op_sel_hi:[1,1]
	v_pk_mul_f32 v[28:29], v[20:21], s[44:45] op_sel:[0,1] op_sel_hi:[1,1]
	v_pk_mul_f32 v[30:31], v[22:23], s[44:45] op_sel:[0,1] op_sel_hi:[1,1]
	v_mfma_f32_32x32x16_f16 v[72:87], v[192:195], v[12:15], v[72:87]
	v_cmp_lt_i32_e64 s[60:61], 0, v108
	v_cmp_lt_i32_e64 s[62:63], 0, v109
	v_cmp_lt_i32_e64 s[64:65], 0, v110
	v_cmp_lt_i32_e64 s[66:67], 0, v111
	v_max_f32_e32 v24, v24, v28
	v_max_f32_e32 v25, v25, v29
	v_max_f32_e32 v26, v26, v30
	v_max_f32_e32 v27, v27, v31
	v_cndmask_b32_e64 v24, 0, v24, s[60:61]
	v_cndmask_b32_e64 v25, 0, v25, s[62:63]
	v_cndmask_b32_e64 v26, 0, v26, s[64:65]
	v_cndmask_b32_e64 v27, 0, v27, s[66:67]
	v_mfma_f32_32x32x16_f16 v[40:55], v[196:199], v[224:227], v[40:55]
	v_cvt_pkrtz_f16_f32 v34, v24, v25
	v_cvt_pkrtz_f16_f32 v35, v26, v27
	ds_write2_b64 v4, v[32:33], v[34:35] offset0:0 offset1:66
	v_pk_mul_f32 v[24:25], v[16:17], s[38:39] op_sel_hi:[1,0]
	v_pk_mul_f32 v[26:27], v[18:19], s[38:39] op_sel_hi:[1,0]
	v_pk_mul_f32 v[28:29], v[20:21], s[46:47] op_sel_hi:[1,0]
	v_pk_mul_f32 v[30:31], v[22:23], s[46:47] op_sel_hi:[1,0]
	v_mfma_f32_32x32x16_f16 v[56:71], v[196:199], v[228:231], v[56:71]
	v_cmp_lt_i32_e64 s[60:61], 0, v112
	v_cmp_lt_i32_e64 s[62:63], 0, v113
	v_cmp_lt_i32_e64 s[64:65], 0, v114
	v_cmp_lt_i32_e64 s[66:67], 0, v115
	v_max_f32_e32 v24, v24, v28
	v_max_f32_e32 v25, v25, v29
	v_max_f32_e32 v26, v26, v30
	v_max_f32_e32 v27, v27, v31
	v_cndmask_b32_e64 v24, 0, v24, s[60:61]
	v_cndmask_b32_e64 v25, 0, v25, s[62:63]
	v_cndmask_b32_e64 v26, 0, v26, s[64:65]
	v_cndmask_b32_e64 v27, 0, v27, s[66:67]
	v_cvt_pkrtz_f16_f32 v32, v24, v25
	v_cvt_pkrtz_f16_f32 v33, v26, v27
	v_pk_mul_f32 v[24:25], v[16:17], s[38:39] op_sel:[0,1] op_sel_hi:[1,1]
	v_pk_mul_f32 v[26:27], v[18:19], s[38:39] op_sel:[0,1] op_sel_hi:[1,1]
	v_pk_mul_f32 v[28:29], v[20:21], s[46:47] op_sel:[0,1] op_sel_hi:[1,1]
	v_pk_mul_f32 v[30:31], v[22:23], s[46:47] op_sel:[0,1] op_sel_hi:[1,1]
	v_mfma_f32_32x32x16_f16 v[72:87], v[196:199], v[12:15], v[72:87]
	v_cmp_lt_i32_e64 s[60:61], 0, v116
	v_cmp_lt_i32_e64 s[62:63], 0, v117
	v_cmp_lt_i32_e64 s[64:65], 0, v118
	v_cmp_lt_i32_e64 s[66:67], 0, v119
	v_max_f32_e32 v24, v24, v28
	v_max_f32_e32 v25, v25, v29
	v_max_f32_e32 v26, v26, v30
	v_max_f32_e32 v27, v27, v31
	v_cndmask_b32_e64 v24, 0, v24, s[60:61]
	v_cndmask_b32_e64 v25, 0, v25, s[62:63]
	v_cndmask_b32_e64 v26, 0, v26, s[64:65]
	v_cndmask_b32_e64 v27, 0, v27, s[66:67]
	v_cvt_pkrtz_f16_f32 v34, v24, v25
	v_cvt_pkrtz_f16_f32 v35, v26, v27
	ds_write2_b64 v4, v[32:33], v[34:35] offset0:132 offset1:198
	ds_write_b128 v9, v[152:155] offset:0
	ds_write_b128 v9, v[156:159] offset:1024
	ds_write_b128 v9, v[160:163] offset:2048
	ds_write_b128 v9, v[164:167] offset:3072
	s_add_u32 s3, s19, 5
	s_and_b32 s3, s3, 7
	s_lshl_b32 s3, s3, 10
	v_add_u32_e32 v11, s3, v10
	ds_read_b128 v[16:19], v11
	ds_read_b128 v[20:23], v11 offset:8192
	s_waitcnt lgkmcnt(0)
	s_barrier
	ds_read_b128 v[184:187], v7 offset:0
	ds_read_b128 v[200:203], v8 offset:0
	ds_read_b128 v[204:207], v8 offset:1024
	ds_read_b128 v[188:191], v7 offset:32
	ds_read_b128 v[208:211], v8 offset:2048
	ds_read_b128 v[212:215], v8 offset:3072
	ds_read_b128 v[192:195], v7 offset:64
	ds_read_b128 v[216:219], v8 offset:4096
	ds_read_b128 v[220:223], v8 offset:5120
	ds_read_b128 v[196:199], v7 offset:96
	ds_read_b128 v[224:227], v8 offset:6144
	ds_read_b128 v[228:231], v8 offset:7168
	s_add_u32 s3, s19, 6
	s_and_b32 s3, s3, 7
	s_lshl_b32 s57, s3, 10
	s_add_u32 s48, s57, s22
	s_add_u32 s49, s48, 0x2000
	s_add_u32 s50, s48, 0x4000
	s_add_u32 s51, s48, 0x6000
	s_add_u32 s52, s48, 0x8000
	s_add_u32 s53, s48, 0xa000
	s_add_u32 s54, s48, 0xc000
	s_add_u32 s55, s48, 0xe000
	s_lshl_b32 s56, s3, 15
	s_add_u32 s56, s56, s23
	buffer_load_dwordx4 v[88:91], v1, s[4:7], s48 offen nt
	buffer_load_dwordx4 v[92:95], v1, s[4:7], s49 offen nt
	buffer_load_dwordx4 v[96:99], v1, s[4:7], s50 offen nt
	buffer_load_dwordx4 v[100:103], v1, s[4:7], s51 offen nt
	buffer_load_dwordx4 v[104:107], v1, s[4:7], s52 offen nt
	buffer_load_dwordx4 v[108:111], v1, s[4:7], s53 offen nt
	buffer_load_dwordx4 v[112:115], v1, s[4:7], s54 offen nt
	buffer_load_dwordx4 v[116:119], v1, s[4:7], s55 offen nt
	buffer_load_dwordx4 v[152:155], v1, s[8:11], s56 offen
	buffer_load_dwordx4 v[156:159], v1, s[8:11], s56 offen offset:1024
	buffer_load_dwordx4 v[160:163], v1, s[8:11], s56 offen offset:2048
	buffer_load_dwordx4 v[164:167], v1, s[8:11], s56 offen offset:3072
	s_waitcnt vmcnt(12)
	v_pk_mul_f32 v[24:25], v[16:17], s[32:33] op_sel_hi:[1,0]
	v_pk_mul_f32 v[26:27], v[18:19], s[32:33] op_sel_hi:[1,0]
	v_pk_mul_f32 v[28:29], v[20:21], s[40:41] op_sel_hi:[1,0]
	v_pk_mul_f32 v[30:31], v[22:23], s[40:41] op_sel_hi:[1,0]
	v_cmp_lt_i32_e64 s[60:61], 0, v120
	v_cmp_lt_i32_e64 s[62:63], 0, v121
	v_cmp_lt_i32_e64 s[64:65], 0, v122
	v_cmp_lt_i32_e64 s[66:67], 0, v123
	v_max_f32_e32 v24, v24, v28
	v_max_f32_e32 v25, v25, v29
	v_max_f32_e32 v26, v26, v30
	v_max_f32_e32 v27, v27, v31
	v_cndmask_b32_e64 v24, 0, v24, s[60:61]
	v_cndmask_b32_e64 v25, 0, v25, s[62:63]
	v_cndmask_b32_e64 v26, 0, v26, s[64:65]
	v_cndmask_b32_e64 v27, 0, v27, s[66:67]
	v_cvt_pkrtz_f16_f32 v32, v24, v25
	v_cvt_pkrtz_f16_f32 v33, v26, v27
	s_waitcnt lgkmcnt(0)
	v_pk_mul_f32 v[24:25], v[16:17], s[32:33] op_sel:[0,1] op_sel_hi:[1,1]
	v_pk_mul_f32 v[26:27], v[18:19], s[32:33] op_sel:[0,1] op_sel_hi:[1,1]
	v_pk_mul_f32 v[28:29], v[20:21], s[40:41] op_sel:[0,1] op_sel_hi:[1,1]
	v_pk_mul_f32 v[30:31], v[22:23], s[40:41] op_sel:[0,1] op_sel_hi:[1,1]
	v_mfma_f32_32x32x16_f16 v[40:55], v[184:187], v[200:203], v[40:55]
	v_cmp_lt_i32_e64 s[60:61], 0, v124
	v_cmp_lt_i32_e64 s[62:63], 0, v125
	v_cmp_lt_i32_e64 s[64:65], 0, v126
	v_cmp_lt_i32_e64 s[66:67], 0, v127
	v_max_f32_e32 v24, v24, v28
	v_max_f32_e32 v25, v25, v29
	v_max_f32_e32 v26, v26, v30
	v_max_f32_e32 v27, v27, v31
	v_cndmask_b32_e64 v24, 0, v24, s[60:61]
	v_cndmask_b32_e64 v25, 0, v25, s[62:63]
	v_cndmask_b32_e64 v26, 0, v26, s[64:65]
	v_cndmask_b32_e64 v27, 0, v27, s[66:67]
	v_mfma_f32_32x32x16_f16 v[56:71], v[184:187], v[204:207], v[56:71]
	v_cvt_pkrtz_f16_f32 v34, v24, v25
	v_cvt_pkrtz_f16_f32 v35, v26, v27
	ds_write2_b64 v5, v[32:33], v[34:35] offset0:0 offset1:66
	v_pk_mul_f32 v[24:25], v[16:17], s[34:35] op_sel_hi:[1,0]
	v_pk_mul_f32 v[26:27], v[18:19], s[34:35] op_sel_hi:[1,0]
	v_pk_mul_f32 v[28:29], v[20:21], s[42:43] op_sel_hi:[1,0]
	v_pk_mul_f32 v[30:31], v[22:23], s[42:43] op_sel_hi:[1,0]
	v_mfma_f32_32x32x16_f16 v[72:87], v[184:187], v[12:15], v[72:87]
	v_cmp_lt_i32_e64 s[60:61], 0, v128
	v_cmp_lt_i32_e64 s[62:63], 0, v129
	v_cmp_lt_i32_e64 s[64:65], 0, v130
	v_cmp_lt_i32_e64 s[66:67], 0, v131
	v_max_f32_e32 v24, v24, v28
	v_max_f32_e32 v25, v25, v29
	v_max_f32_e32 v26, v26, v30
	v_max_f32_e32 v27, v27, v31
	v_cndmask_b32_e64 v24, 0, v24, s[60:61]
	v_cndmask_b32_e64 v25, 0, v25, s[62:63]
	v_cndmask_b32_e64 v26, 0, v26, s[64:65]
	v_cndmask_b32_e64 v27, 0, v27, s[66:67]
	v_mfma_f32_32x32x16_f16 v[40:55], v[188:191], v[208:211], v[40:55]
	v_cvt_pkrtz_f16_f32 v32, v24, v25
	v_cvt_pkrtz_f16_f32 v33, v26, v27
	v_pk_mul_f32 v[24:25], v[16:17], s[34:35] op_sel:[0,1] op_sel_hi:[1,1]
	v_pk_mul_f32 v[26:27], v[18:19], s[34:35] op_sel:[0,1] op_sel_hi:[1,1]
	v_pk_mul_f32 v[28:29], v[20:21], s[42:43] op_sel:[0,1] op_sel_hi:[1,1]
	v_pk_mul_f32 v[30:31], v[22:23], s[42:43] op_sel:[0,1] op_sel_hi:[1,1]
	v_mfma_f32_32x32x16_f16 v[56:71], v[188:191], v[212:215], v[56:71]
	v_cmp_lt_i32_e64 s[60:61], 0, v132
	v_cmp_lt_i32_e64 s[62:63], 0, v133
	v_cmp_lt_i32_e64 s[64:65], 0, v134
	v_cmp_lt_i32_e64 s[66:67], 0, v135
	v_max_f32_e32 v24, v24, v28
	v_max_f32_e32 v25, v25, v29
	v_max_f32_e32 v26, v26, v30
	v_max_f32_e32 v27, v27, v31
	v_cndmask_b32_e64 v24, 0, v24, s[60:61]
	v_cndmask_b32_e64 v25, 0, v25, s[62:63]
	v_cndmask_b32_e64 v26, 0, v26, s[64:65]
	v_cndmask_b32_e64 v27, 0, v27, s[66:67]
	v_mfma_f32_32x32x16_f16 v[72:87], v[188:191], v[12:15], v[72:87]
	v_cvt_pkrtz_f16_f32 v34, v24, v25
	v_cvt_pkrtz_f16_f32 v35, v26, v27
	ds_write2_b64 v5, v[32:33], v[34:35] offset0:132 offset1:198
	v_pk_mul_f32 v[24:25], v[16:17], s[36:37] op_sel_hi:[1,0]
	v_pk_mul_f32 v[26:27], v[18:19], s[36:37] op_sel_hi:[1,0]
	v_pk_mul_f32 v[28:29], v[20:21], s[44:45] op_sel_hi:[1,0]
	v_pk_mul_f32 v[30:31], v[22:23], s[44:45] op_sel_hi:[1,0]
	v_mfma_f32_32x32x16_f16 v[40:55], v[192:195], v[216:219], v[40:55]
	v_cmp_lt_i32_e64 s[60:61], 0, v136
	v_cmp_lt_i32_e64 s[62:63], 0, v137
	v_cmp_lt_i32_e64 s[64:65], 0, v138
	v_cmp_lt_i32_e64 s[66:67], 0, v139
	v_max_f32_e32 v24, v24, v28
	v_max_f32_e32 v25, v25, v29
	v_max_f32_e32 v26, v26, v30
	v_max_f32_e32 v27, v27, v31
	v_cndmask_b32_e64 v24, 0, v24, s[60:61]
	v_cndmask_b32_e64 v25, 0, v25, s[62:63]
	v_cndmask_b32_e64 v26, 0, v26, s[64:65]
	v_cndmask_b32_e64 v27, 0, v27, s[66:67]
	v_mfma_f32_32x32x16_f16 v[56:71], v[192:195], v[220:223], v[56:71]
	v_cvt_pkrtz_f16_f32 v32, v24, v25
	v_cvt_pkrtz_f16_f32 v33, v26, v27
	v_pk_mul_f32 v[24:25], v[16:17], s[36:37] op_sel:[0,1] op_sel_hi:[1,1]
	v_pk_mul_f32 v[26:27], v[18:19], s[36:37] op_sel:[0,1] op_sel_hi:[1,1]
	v_pk_mul_f32 v[28:29], v[20:21], s[44:45] op_sel:[0,1] op_sel_hi:[1,1]
	v_pk_mul_f32 v[30:31], v[22:23], s[44:45] op_sel:[0,1] op_sel_hi:[1,1]
	v_mfma_f32_32x32x16_f16 v[72:87], v[192:195], v[12:15], v[72:87]
	v_cmp_lt_i32_e64 s[60:61], 0, v140
	v_cmp_lt_i32_e64 s[62:63], 0, v141
	v_cmp_lt_i32_e64 s[64:65], 0, v142
	v_cmp_lt_i32_e64 s[66:67], 0, v143
	v_max_f32_e32 v24, v24, v28
	v_max_f32_e32 v25, v25, v29
	v_max_f32_e32 v26, v26, v30
	v_max_f32_e32 v27, v27, v31
	v_cndmask_b32_e64 v24, 0, v24, s[60:61]
	v_cndmask_b32_e64 v25, 0, v25, s[62:63]
	v_cndmask_b32_e64 v26, 0, v26, s[64:65]
	v_cndmask_b32_e64 v27, 0, v27, s[66:67]
	v_mfma_f32_32x32x16_f16 v[40:55], v[196:199], v[224:227], v[40:55]
	v_cvt_pkrtz_f16_f32 v34, v24, v25
	v_cvt_pkrtz_f16_f32 v35, v26, v27
	ds_write2_b64 v6, v[32:33], v[34:35] offset0:0 offset1:66
	v_pk_mul_f32 v[24:25], v[16:17], s[38:39] op_sel_hi:[1,0]
	v_pk_mul_f32 v[26:27], v[18:19], s[38:39] op_sel_hi:[1,0]
	v_pk_mul_f32 v[28:29], v[20:21], s[46:47] op_sel_hi:[1,0]
	v_pk_mul_f32 v[30:31], v[22:23], s[46:47] op_sel_hi:[1,0]
	v_mfma_f32_32x32x16_f16 v[56:71], v[196:199], v[228:231], v[56:71]
	v_cmp_lt_i32_e64 s[60:61], 0, v144
	v_cmp_lt_i32_e64 s[62:63], 0, v145
	v_cmp_lt_i32_e64 s[64:65], 0, v146
	v_cmp_lt_i32_e64 s[66:67], 0, v147
	v_max_f32_e32 v24, v24, v28
	v_max_f32_e32 v25, v25, v29
	v_max_f32_e32 v26, v26, v30
	v_max_f32_e32 v27, v27, v31
	v_cndmask_b32_e64 v24, 0, v24, s[60:61]
	v_cndmask_b32_e64 v25, 0, v25, s[62:63]
	v_cndmask_b32_e64 v26, 0, v26, s[64:65]
	v_cndmask_b32_e64 v27, 0, v27, s[66:67]
	v_cvt_pkrtz_f16_f32 v32, v24, v25
	v_cvt_pkrtz_f16_f32 v33, v26, v27
	v_pk_mul_f32 v[24:25], v[16:17], s[38:39] op_sel:[0,1] op_sel_hi:[1,1]
	v_pk_mul_f32 v[26:27], v[18:19], s[38:39] op_sel:[0,1] op_sel_hi:[1,1]
	v_pk_mul_f32 v[28:29], v[20:21], s[46:47] op_sel:[0,1] op_sel_hi:[1,1]
	v_pk_mul_f32 v[30:31], v[22:23], s[46:47] op_sel:[0,1] op_sel_hi:[1,1]
	v_mfma_f32_32x32x16_f16 v[72:87], v[196:199], v[12:15], v[72:87]
	v_cmp_lt_i32_e64 s[60:61], 0, v148
	v_cmp_lt_i32_e64 s[62:63], 0, v149
	v_cmp_lt_i32_e64 s[64:65], 0, v150
	v_cmp_lt_i32_e64 s[66:67], 0, v151
	v_max_f32_e32 v24, v24, v28
	v_max_f32_e32 v25, v25, v29
	v_max_f32_e32 v26, v26, v30
	v_max_f32_e32 v27, v27, v31
	v_cndmask_b32_e64 v24, 0, v24, s[60:61]
	v_cndmask_b32_e64 v25, 0, v25, s[62:63]
	v_cndmask_b32_e64 v26, 0, v26, s[64:65]
	v_cndmask_b32_e64 v27, 0, v27, s[66:67]
	v_cvt_pkrtz_f16_f32 v34, v24, v25
	v_cvt_pkrtz_f16_f32 v35, v26, v27
	ds_write2_b64 v6, v[32:33], v[34:35] offset0:132 offset1:198
	ds_write_b128 v9, v[168:171] offset:32768
	ds_write_b128 v9, v[172:175] offset:33792
	ds_write_b128 v9, v[176:179] offset:34816
	ds_write_b128 v9, v[180:183] offset:35840
	s_add_u32 s3, s19, 6
	s_and_b32 s3, s3, 7
	s_lshl_b32 s3, s3, 10
	v_add_u32_e32 v11, s3, v10
	ds_read_b128 v[16:19], v11
	ds_read_b128 v[20:23], v11 offset:8192
	s_waitcnt lgkmcnt(0)
	s_barrier
	ds_read_b128 v[184:187], v7 offset:33792
	ds_read_b128 v[200:203], v8 offset:32768
	ds_read_b128 v[204:207], v8 offset:33792
	ds_read_b128 v[188:191], v7 offset:33824
	ds_read_b128 v[208:211], v8 offset:34816
	ds_read_b128 v[212:215], v8 offset:35840
	ds_read_b128 v[192:195], v7 offset:33856
	ds_read_b128 v[216:219], v8 offset:36864
	ds_read_b128 v[220:223], v8 offset:37888
	ds_read_b128 v[196:199], v7 offset:33888
	ds_read_b128 v[224:227], v8 offset:38912
	ds_read_b128 v[228:231], v8 offset:39936
	s_add_u32 s3, s19, 7
	s_and_b32 s3, s3, 7
	s_lshl_b32 s57, s3, 10
	s_add_u32 s48, s57, s22
	s_add_u32 s49, s48, 0x2000
	s_add_u32 s50, s48, 0x4000
	s_add_u32 s51, s48, 0x6000
	s_add_u32 s52, s48, 0x8000
	s_add_u32 s53, s48, 0xa000
	s_add_u32 s54, s48, 0xc000
	s_add_u32 s55, s48, 0xe000
	s_lshl_b32 s56, s3, 15
	s_add_u32 s56, s56, s23
	buffer_load_dwordx4 v[120:123], v1, s[4:7], s48 offen nt
	buffer_load_dwordx4 v[124:127], v1, s[4:7], s49 offen nt
	buffer_load_dwordx4 v[128:131], v1, s[4:7], s50 offen nt
	buffer_load_dwordx4 v[132:135], v1, s[4:7], s51 offen nt
	buffer_load_dwordx4 v[136:139], v1, s[4:7], s52 offen nt
	buffer_load_dwordx4 v[140:143], v1, s[4:7], s53 offen nt
	buffer_load_dwordx4 v[144:147], v1, s[4:7], s54 offen nt
	buffer_load_dwordx4 v[148:151], v1, s[4:7], s55 offen nt
	buffer_load_dwordx4 v[168:171], v1, s[8:11], s56 offen
	buffer_load_dwordx4 v[172:175], v1, s[8:11], s56 offen offset:1024
	buffer_load_dwordx4 v[176:179], v1, s[8:11], s56 offen offset:2048
	buffer_load_dwordx4 v[180:183], v1, s[8:11], s56 offen offset:3072
	s_waitcnt vmcnt(12)
	v_pk_mul_f32 v[24:25], v[16:17], s[32:33] op_sel_hi:[1,0]
	v_pk_mul_f32 v[26:27], v[18:19], s[32:33] op_sel_hi:[1,0]
	v_pk_mul_f32 v[28:29], v[20:21], s[40:41] op_sel_hi:[1,0]
	v_pk_mul_f32 v[30:31], v[22:23], s[40:41] op_sel_hi:[1,0]
	v_cmp_lt_i32_e64 s[60:61], 0, v88
	v_cmp_lt_i32_e64 s[62:63], 0, v89
	v_cmp_lt_i32_e64 s[64:65], 0, v90
	v_cmp_lt_i32_e64 s[66:67], 0, v91
	v_max_f32_e32 v24, v24, v28
	v_max_f32_e32 v25, v25, v29
	v_max_f32_e32 v26, v26, v30
	v_max_f32_e32 v27, v27, v31
	v_cndmask_b32_e64 v24, 0, v24, s[60:61]
	v_cndmask_b32_e64 v25, 0, v25, s[62:63]
	v_cndmask_b32_e64 v26, 0, v26, s[64:65]
	v_cndmask_b32_e64 v27, 0, v27, s[66:67]
	v_cvt_pkrtz_f16_f32 v32, v24, v25
	v_cvt_pkrtz_f16_f32 v33, v26, v27
	s_waitcnt lgkmcnt(0)
	v_pk_mul_f32 v[24:25], v[16:17], s[32:33] op_sel:[0,1] op_sel_hi:[1,1]
	v_pk_mul_f32 v[26:27], v[18:19], s[32:33] op_sel:[0,1] op_sel_hi:[1,1]
	v_pk_mul_f32 v[28:29], v[20:21], s[40:41] op_sel:[0,1] op_sel_hi:[1,1]
	v_pk_mul_f32 v[30:31], v[22:23], s[40:41] op_sel:[0,1] op_sel_hi:[1,1]
	v_mfma_f32_32x32x16_f16 v[40:55], v[184:187], v[200:203], v[40:55]
	v_cmp_lt_i32_e64 s[60:61], 0, v92
	v_cmp_lt_i32_e64 s[62:63], 0, v93
	v_cmp_lt_i32_e64 s[64:65], 0, v94
	v_cmp_lt_i32_e64 s[66:67], 0, v95
	v_max_f32_e32 v24, v24, v28
	v_max_f32_e32 v25, v25, v29
	v_max_f32_e32 v26, v26, v30
	v_max_f32_e32 v27, v27, v31
	v_cndmask_b32_e64 v24, 0, v24, s[60:61]
	v_cndmask_b32_e64 v25, 0, v25, s[62:63]
	v_cndmask_b32_e64 v26, 0, v26, s[64:65]
	v_cndmask_b32_e64 v27, 0, v27, s[66:67]
	v_mfma_f32_32x32x16_f16 v[56:71], v[184:187], v[204:207], v[56:71]
	v_cvt_pkrtz_f16_f32 v34, v24, v25
	v_cvt_pkrtz_f16_f32 v35, v26, v27
	ds_write2_b64 v3, v[32:33], v[34:35] offset0:0 offset1:66
	v_pk_mul_f32 v[24:25], v[16:17], s[34:35] op_sel_hi:[1,0]
	v_pk_mul_f32 v[26:27], v[18:19], s[34:35] op_sel_hi:[1,0]
	v_pk_mul_f32 v[28:29], v[20:21], s[42:43] op_sel_hi:[1,0]
	v_pk_mul_f32 v[30:31], v[22:23], s[42:43] op_sel_hi:[1,0]
	v_mfma_f32_32x32x16_f16 v[72:87], v[184:187], v[12:15], v[72:87]
	v_cmp_lt_i32_e64 s[60:61], 0, v96
	v_cmp_lt_i32_e64 s[62:63], 0, v97
	v_cmp_lt_i32_e64 s[64:65], 0, v98
	v_cmp_lt_i32_e64 s[66:67], 0, v99
	v_max_f32_e32 v24, v24, v28
	v_max_f32_e32 v25, v25, v29
	v_max_f32_e32 v26, v26, v30
	v_max_f32_e32 v27, v27, v31
	v_cndmask_b32_e64 v24, 0, v24, s[60:61]
	v_cndmask_b32_e64 v25, 0, v25, s[62:63]
	v_cndmask_b32_e64 v26, 0, v26, s[64:65]
	v_cndmask_b32_e64 v27, 0, v27, s[66:67]
	v_mfma_f32_32x32x16_f16 v[40:55], v[188:191], v[208:211], v[40:55]
	v_cvt_pkrtz_f16_f32 v32, v24, v25
	v_cvt_pkrtz_f16_f32 v33, v26, v27
	v_pk_mul_f32 v[24:25], v[16:17], s[34:35] op_sel:[0,1] op_sel_hi:[1,1]
	v_pk_mul_f32 v[26:27], v[18:19], s[34:35] op_sel:[0,1] op_sel_hi:[1,1]
	v_pk_mul_f32 v[28:29], v[20:21], s[42:43] op_sel:[0,1] op_sel_hi:[1,1]
	v_pk_mul_f32 v[30:31], v[22:23], s[42:43] op_sel:[0,1] op_sel_hi:[1,1]
	v_mfma_f32_32x32x16_f16 v[56:71], v[188:191], v[212:215], v[56:71]
	v_cmp_lt_i32_e64 s[60:61], 0, v100
	v_cmp_lt_i32_e64 s[62:63], 0, v101
	v_cmp_lt_i32_e64 s[64:65], 0, v102
	v_cmp_lt_i32_e64 s[66:67], 0, v103
	v_max_f32_e32 v24, v24, v28
	v_max_f32_e32 v25, v25, v29
	v_max_f32_e32 v26, v26, v30
	v_max_f32_e32 v27, v27, v31
	v_cndmask_b32_e64 v24, 0, v24, s[60:61]
	v_cndmask_b32_e64 v25, 0, v25, s[62:63]
	v_cndmask_b32_e64 v26, 0, v26, s[64:65]
	v_cndmask_b32_e64 v27, 0, v27, s[66:67]
	v_mfma_f32_32x32x16_f16 v[72:87], v[188:191], v[12:15], v[72:87]
	v_cvt_pkrtz_f16_f32 v34, v24, v25
	v_cvt_pkrtz_f16_f32 v35, v26, v27
	ds_write2_b64 v3, v[32:33], v[34:35] offset0:132 offset1:198
	v_pk_mul_f32 v[24:25], v[16:17], s[36:37] op_sel_hi:[1,0]
	v_pk_mul_f32 v[26:27], v[18:19], s[36:37] op_sel_hi:[1,0]
	v_pk_mul_f32 v[28:29], v[20:21], s[44:45] op_sel_hi:[1,0]
	v_pk_mul_f32 v[30:31], v[22:23], s[44:45] op_sel_hi:[1,0]
	v_mfma_f32_32x32x16_f16 v[40:55], v[192:195], v[216:219], v[40:55]
	v_cmp_lt_i32_e64 s[60:61], 0, v104
	v_cmp_lt_i32_e64 s[62:63], 0, v105
	v_cmp_lt_i32_e64 s[64:65], 0, v106
	v_cmp_lt_i32_e64 s[66:67], 0, v107
	v_max_f32_e32 v24, v24, v28
	v_max_f32_e32 v25, v25, v29
	v_max_f32_e32 v26, v26, v30
	v_max_f32_e32 v27, v27, v31
	v_cndmask_b32_e64 v24, 0, v24, s[60:61]
	v_cndmask_b32_e64 v25, 0, v25, s[62:63]
	v_cndmask_b32_e64 v26, 0, v26, s[64:65]
	v_cndmask_b32_e64 v27, 0, v27, s[66:67]
	v_mfma_f32_32x32x16_f16 v[56:71], v[192:195], v[220:223], v[56:71]
	v_cvt_pkrtz_f16_f32 v32, v24, v25
	v_cvt_pkrtz_f16_f32 v33, v26, v27
	v_pk_mul_f32 v[24:25], v[16:17], s[36:37] op_sel:[0,1] op_sel_hi:[1,1]
	v_pk_mul_f32 v[26:27], v[18:19], s[36:37] op_sel:[0,1] op_sel_hi:[1,1]
	v_pk_mul_f32 v[28:29], v[20:21], s[44:45] op_sel:[0,1] op_sel_hi:[1,1]
	v_pk_mul_f32 v[30:31], v[22:23], s[44:45] op_sel:[0,1] op_sel_hi:[1,1]
	v_mfma_f32_32x32x16_f16 v[72:87], v[192:195], v[12:15], v[72:87]
	v_cmp_lt_i32_e64 s[60:61], 0, v108
	v_cmp_lt_i32_e64 s[62:63], 0, v109
	v_cmp_lt_i32_e64 s[64:65], 0, v110
	v_cmp_lt_i32_e64 s[66:67], 0, v111
	v_max_f32_e32 v24, v24, v28
	v_max_f32_e32 v25, v25, v29
	v_max_f32_e32 v26, v26, v30
	v_max_f32_e32 v27, v27, v31
	v_cndmask_b32_e64 v24, 0, v24, s[60:61]
	v_cndmask_b32_e64 v25, 0, v25, s[62:63]
	v_cndmask_b32_e64 v26, 0, v26, s[64:65]
	v_cndmask_b32_e64 v27, 0, v27, s[66:67]
	v_mfma_f32_32x32x16_f16 v[40:55], v[196:199], v[224:227], v[40:55]
	v_cvt_pkrtz_f16_f32 v34, v24, v25
	v_cvt_pkrtz_f16_f32 v35, v26, v27
	ds_write2_b64 v4, v[32:33], v[34:35] offset0:0 offset1:66
	v_pk_mul_f32 v[24:25], v[16:17], s[38:39] op_sel_hi:[1,0]
	v_pk_mul_f32 v[26:27], v[18:19], s[38:39] op_sel_hi:[1,0]
	v_pk_mul_f32 v[28:29], v[20:21], s[46:47] op_sel_hi:[1,0]
	v_pk_mul_f32 v[30:31], v[22:23], s[46:47] op_sel_hi:[1,0]
	v_mfma_f32_32x32x16_f16 v[56:71], v[196:199], v[228:231], v[56:71]
	v_cmp_lt_i32_e64 s[60:61], 0, v112
	v_cmp_lt_i32_e64 s[62:63], 0, v113
	v_cmp_lt_i32_e64 s[64:65], 0, v114
	v_cmp_lt_i32_e64 s[66:67], 0, v115
	v_max_f32_e32 v24, v24, v28
	v_max_f32_e32 v25, v25, v29
	v_max_f32_e32 v26, v26, v30
	v_max_f32_e32 v27, v27, v31
	v_cndmask_b32_e64 v24, 0, v24, s[60:61]
	v_cndmask_b32_e64 v25, 0, v25, s[62:63]
	v_cndmask_b32_e64 v26, 0, v26, s[64:65]
	v_cndmask_b32_e64 v27, 0, v27, s[66:67]
	v_cvt_pkrtz_f16_f32 v32, v24, v25
	v_cvt_pkrtz_f16_f32 v33, v26, v27
	v_pk_mul_f32 v[24:25], v[16:17], s[38:39] op_sel:[0,1] op_sel_hi:[1,1]
	v_pk_mul_f32 v[26:27], v[18:19], s[38:39] op_sel:[0,1] op_sel_hi:[1,1]
	v_pk_mul_f32 v[28:29], v[20:21], s[46:47] op_sel:[0,1] op_sel_hi:[1,1]
	v_pk_mul_f32 v[30:31], v[22:23], s[46:47] op_sel:[0,1] op_sel_hi:[1,1]
	v_mfma_f32_32x32x16_f16 v[72:87], v[196:199], v[12:15], v[72:87]
	v_cmp_lt_i32_e64 s[60:61], 0, v116
	v_cmp_lt_i32_e64 s[62:63], 0, v117
	v_cmp_lt_i32_e64 s[64:65], 0, v118
	v_cmp_lt_i32_e64 s[66:67], 0, v119
	v_max_f32_e32 v24, v24, v28
	v_max_f32_e32 v25, v25, v29
	v_max_f32_e32 v26, v26, v30
	v_max_f32_e32 v27, v27, v31
	v_cndmask_b32_e64 v24, 0, v24, s[60:61]
	v_cndmask_b32_e64 v25, 0, v25, s[62:63]
	v_cndmask_b32_e64 v26, 0, v26, s[64:65]
	v_cndmask_b32_e64 v27, 0, v27, s[66:67]
	v_cvt_pkrtz_f16_f32 v34, v24, v25
	v_cvt_pkrtz_f16_f32 v35, v26, v27
	ds_write2_b64 v4, v[32:33], v[34:35] offset0:132 offset1:198
	ds_write_b128 v9, v[152:155] offset:0
	ds_write_b128 v9, v[156:159] offset:1024
	ds_write_b128 v9, v[160:163] offset:2048
	ds_write_b128 v9, v[164:167] offset:3072
	s_add_u32 s3, s19, 7
	s_and_b32 s3, s3, 7
	s_lshl_b32 s3, s3, 10
	v_add_u32_e32 v11, s3, v10
	ds_read_b128 v[16:19], v11
	ds_read_b128 v[20:23], v11 offset:8192
	s_waitcnt lgkmcnt(0)
	s_barrier
	ds_read_b128 v[184:187], v7 offset:0
	ds_read_b128 v[200:203], v8 offset:0
	ds_read_b128 v[204:207], v8 offset:1024
	ds_read_b128 v[188:191], v7 offset:32
	ds_read_b128 v[208:211], v8 offset:2048
	ds_read_b128 v[212:215], v8 offset:3072
	ds_read_b128 v[192:195], v7 offset:64
	ds_read_b128 v[216:219], v8 offset:4096
	ds_read_b128 v[220:223], v8 offset:5120
	ds_read_b128 v[196:199], v7 offset:96
	ds_read_b128 v[224:227], v8 offset:6144
	ds_read_b128 v[228:231], v8 offset:7168
	s_waitcnt vmcnt(0)
	v_pk_mul_f32 v[24:25], v[16:17], s[32:33] op_sel_hi:[1,0]
	v_pk_mul_f32 v[26:27], v[18:19], s[32:33] op_sel_hi:[1,0]
	v_pk_mul_f32 v[28:29], v[20:21], s[40:41] op_sel_hi:[1,0]
	v_pk_mul_f32 v[30:31], v[22:23], s[40:41] op_sel_hi:[1,0]
	v_cmp_lt_i32_e64 s[60:61], 0, v120
	v_cmp_lt_i32_e64 s[62:63], 0, v121
	v_cmp_lt_i32_e64 s[64:65], 0, v122
	v_cmp_lt_i32_e64 s[66:67], 0, v123
	v_max_f32_e32 v24, v24, v28
	v_max_f32_e32 v25, v25, v29
	v_max_f32_e32 v26, v26, v30
	v_max_f32_e32 v27, v27, v31
	v_cndmask_b32_e64 v24, 0, v24, s[60:61]
	v_cndmask_b32_e64 v25, 0, v25, s[62:63]
	v_cndmask_b32_e64 v26, 0, v26, s[64:65]
	v_cndmask_b32_e64 v27, 0, v27, s[66:67]
	v_cvt_pkrtz_f16_f32 v32, v24, v25
	v_cvt_pkrtz_f16_f32 v33, v26, v27
	s_waitcnt lgkmcnt(0)
	v_pk_mul_f32 v[24:25], v[16:17], s[32:33] op_sel:[0,1] op_sel_hi:[1,1]
	v_pk_mul_f32 v[26:27], v[18:19], s[32:33] op_sel:[0,1] op_sel_hi:[1,1]
	v_pk_mul_f32 v[28:29], v[20:21], s[40:41] op_sel:[0,1] op_sel_hi:[1,1]
	v_pk_mul_f32 v[30:31], v[22:23], s[40:41] op_sel:[0,1] op_sel_hi:[1,1]
	v_mfma_f32_32x32x16_f16 v[40:55], v[184:187], v[200:203], v[40:55]
	v_cmp_lt_i32_e64 s[60:61], 0, v124
	v_cmp_lt_i32_e64 s[62:63], 0, v125
	v_cmp_lt_i32_e64 s[64:65], 0, v126
	v_cmp_lt_i32_e64 s[66:67], 0, v127
	v_max_f32_e32 v24, v24, v28
	v_max_f32_e32 v25, v25, v29
	v_max_f32_e32 v26, v26, v30
	v_max_f32_e32 v27, v27, v31
	v_cndmask_b32_e64 v24, 0, v24, s[60:61]
	v_cndmask_b32_e64 v25, 0, v25, s[62:63]
	v_cndmask_b32_e64 v26, 0, v26, s[64:65]
	v_cndmask_b32_e64 v27, 0, v27, s[66:67]
	v_mfma_f32_32x32x16_f16 v[56:71], v[184:187], v[204:207], v[56:71]
	v_cvt_pkrtz_f16_f32 v34, v24, v25
	v_cvt_pkrtz_f16_f32 v35, v26, v27
	ds_write2_b64 v5, v[32:33], v[34:35] offset0:0 offset1:66
	v_pk_mul_f32 v[24:25], v[16:17], s[34:35] op_sel_hi:[1,0]
	v_pk_mul_f32 v[26:27], v[18:19], s[34:35] op_sel_hi:[1,0]
	v_pk_mul_f32 v[28:29], v[20:21], s[42:43] op_sel_hi:[1,0]
	v_pk_mul_f32 v[30:31], v[22:23], s[42:43] op_sel_hi:[1,0]
	v_mfma_f32_32x32x16_f16 v[72:87], v[184:187], v[12:15], v[72:87]
	v_cmp_lt_i32_e64 s[60:61], 0, v128
	v_cmp_lt_i32_e64 s[62:63], 0, v129
	v_cmp_lt_i32_e64 s[64:65], 0, v130
	v_cmp_lt_i32_e64 s[66:67], 0, v131
	v_max_f32_e32 v24, v24, v28
	v_max_f32_e32 v25, v25, v29
	v_max_f32_e32 v26, v26, v30
	v_max_f32_e32 v27, v27, v31
	v_cndmask_b32_e64 v24, 0, v24, s[60:61]
	v_cndmask_b32_e64 v25, 0, v25, s[62:63]
	v_cndmask_b32_e64 v26, 0, v26, s[64:65]
	v_cndmask_b32_e64 v27, 0, v27, s[66:67]
	v_mfma_f32_32x32x16_f16 v[40:55], v[188:191], v[208:211], v[40:55]
	v_cvt_pkrtz_f16_f32 v32, v24, v25
	v_cvt_pkrtz_f16_f32 v33, v26, v27
	v_pk_mul_f32 v[24:25], v[16:17], s[34:35] op_sel:[0,1] op_sel_hi:[1,1]
	v_pk_mul_f32 v[26:27], v[18:19], s[34:35] op_sel:[0,1] op_sel_hi:[1,1]
	v_pk_mul_f32 v[28:29], v[20:21], s[42:43] op_sel:[0,1] op_sel_hi:[1,1]
	v_pk_mul_f32 v[30:31], v[22:23], s[42:43] op_sel:[0,1] op_sel_hi:[1,1]
	v_mfma_f32_32x32x16_f16 v[56:71], v[188:191], v[212:215], v[56:71]
	v_cmp_lt_i32_e64 s[60:61], 0, v132
	v_cmp_lt_i32_e64 s[62:63], 0, v133
	v_cmp_lt_i32_e64 s[64:65], 0, v134
	v_cmp_lt_i32_e64 s[66:67], 0, v135
	v_max_f32_e32 v24, v24, v28
	v_max_f32_e32 v25, v25, v29
	v_max_f32_e32 v26, v26, v30
	v_max_f32_e32 v27, v27, v31
	v_cndmask_b32_e64 v24, 0, v24, s[60:61]
	v_cndmask_b32_e64 v25, 0, v25, s[62:63]
	v_cndmask_b32_e64 v26, 0, v26, s[64:65]
	v_cndmask_b32_e64 v27, 0, v27, s[66:67]
	v_mfma_f32_32x32x16_f16 v[72:87], v[188:191], v[12:15], v[72:87]
	v_cvt_pkrtz_f16_f32 v34, v24, v25
	v_cvt_pkrtz_f16_f32 v35, v26, v27
	ds_write2_b64 v5, v[32:33], v[34:35] offset0:132 offset1:198
	v_pk_mul_f32 v[24:25], v[16:17], s[36:37] op_sel_hi:[1,0]
	v_pk_mul_f32 v[26:27], v[18:19], s[36:37] op_sel_hi:[1,0]
	v_pk_mul_f32 v[28:29], v[20:21], s[44:45] op_sel_hi:[1,0]
	v_pk_mul_f32 v[30:31], v[22:23], s[44:45] op_sel_hi:[1,0]
	v_mfma_f32_32x32x16_f16 v[40:55], v[192:195], v[216:219], v[40:55]
	v_cmp_lt_i32_e64 s[60:61], 0, v136
	v_cmp_lt_i32_e64 s[62:63], 0, v137
	v_cmp_lt_i32_e64 s[64:65], 0, v138
	v_cmp_lt_i32_e64 s[66:67], 0, v139
	v_max_f32_e32 v24, v24, v28
	v_max_f32_e32 v25, v25, v29
	v_max_f32_e32 v26, v26, v30
	v_max_f32_e32 v27, v27, v31
	v_cndmask_b32_e64 v24, 0, v24, s[60:61]
	v_cndmask_b32_e64 v25, 0, v25, s[62:63]
	v_cndmask_b32_e64 v26, 0, v26, s[64:65]
	v_cndmask_b32_e64 v27, 0, v27, s[66:67]
	v_mfma_f32_32x32x16_f16 v[56:71], v[192:195], v[220:223], v[56:71]
	v_cvt_pkrtz_f16_f32 v32, v24, v25
	v_cvt_pkrtz_f16_f32 v33, v26, v27
	v_pk_mul_f32 v[24:25], v[16:17], s[36:37] op_sel:[0,1] op_sel_hi:[1,1]
	v_pk_mul_f32 v[26:27], v[18:19], s[36:37] op_sel:[0,1] op_sel_hi:[1,1]
	v_pk_mul_f32 v[28:29], v[20:21], s[44:45] op_sel:[0,1] op_sel_hi:[1,1]
	v_pk_mul_f32 v[30:31], v[22:23], s[44:45] op_sel:[0,1] op_sel_hi:[1,1]
	v_mfma_f32_32x32x16_f16 v[72:87], v[192:195], v[12:15], v[72:87]
	v_cmp_lt_i32_e64 s[60:61], 0, v140
	v_cmp_lt_i32_e64 s[62:63], 0, v141
	v_cmp_lt_i32_e64 s[64:65], 0, v142
	v_cmp_lt_i32_e64 s[66:67], 0, v143
	v_max_f32_e32 v24, v24, v28
	v_max_f32_e32 v25, v25, v29
	v_max_f32_e32 v26, v26, v30
	v_max_f32_e32 v27, v27, v31
	v_cndmask_b32_e64 v24, 0, v24, s[60:61]
	v_cndmask_b32_e64 v25, 0, v25, s[62:63]
	v_cndmask_b32_e64 v26, 0, v26, s[64:65]
	v_cndmask_b32_e64 v27, 0, v27, s[66:67]
	v_mfma_f32_32x32x16_f16 v[40:55], v[196:199], v[224:227], v[40:55]
	v_cvt_pkrtz_f16_f32 v34, v24, v25
	v_cvt_pkrtz_f16_f32 v35, v26, v27
	ds_write2_b64 v6, v[32:33], v[34:35] offset0:0 offset1:66
	v_pk_mul_f32 v[24:25], v[16:17], s[38:39] op_sel_hi:[1,0]
	v_pk_mul_f32 v[26:27], v[18:19], s[38:39] op_sel_hi:[1,0]
	v_pk_mul_f32 v[28:29], v[20:21], s[46:47] op_sel_hi:[1,0]
	v_pk_mul_f32 v[30:31], v[22:23], s[46:47] op_sel_hi:[1,0]
	v_mfma_f32_32x32x16_f16 v[56:71], v[196:199], v[228:231], v[56:71]
	v_cmp_lt_i32_e64 s[60:61], 0, v144
	v_cmp_lt_i32_e64 s[62:63], 0, v145
	v_cmp_lt_i32_e64 s[64:65], 0, v146
	v_cmp_lt_i32_e64 s[66:67], 0, v147
	v_max_f32_e32 v24, v24, v28
	v_max_f32_e32 v25, v25, v29
	v_max_f32_e32 v26, v26, v30
	v_max_f32_e32 v27, v27, v31
	v_cndmask_b32_e64 v24, 0, v24, s[60:61]
	v_cndmask_b32_e64 v25, 0, v25, s[62:63]
	v_cndmask_b32_e64 v26, 0, v26, s[64:65]
	v_cndmask_b32_e64 v27, 0, v27, s[66:67]
	v_cvt_pkrtz_f16_f32 v32, v24, v25
	v_cvt_pkrtz_f16_f32 v33, v26, v27
	v_pk_mul_f32 v[24:25], v[16:17], s[38:39] op_sel:[0,1] op_sel_hi:[1,1]
	v_pk_mul_f32 v[26:27], v[18:19], s[38:39] op_sel:[0,1] op_sel_hi:[1,1]
	v_pk_mul_f32 v[28:29], v[20:21], s[46:47] op_sel:[0,1] op_sel_hi:[1,1]
	v_pk_mul_f32 v[30:31], v[22:23], s[46:47] op_sel:[0,1] op_sel_hi:[1,1]
	v_mfma_f32_32x32x16_f16 v[72:87], v[196:199], v[12:15], v[72:87]
	v_cmp_lt_i32_e64 s[60:61], 0, v148
	v_cmp_lt_i32_e64 s[62:63], 0, v149
	v_cmp_lt_i32_e64 s[64:65], 0, v150
	v_cmp_lt_i32_e64 s[66:67], 0, v151
	v_max_f32_e32 v24, v24, v28
	v_max_f32_e32 v25, v25, v29
	v_max_f32_e32 v26, v26, v30
	v_max_f32_e32 v27, v27, v31
	v_cndmask_b32_e64 v24, 0, v24, s[60:61]
	v_cndmask_b32_e64 v25, 0, v25, s[62:63]
	v_cndmask_b32_e64 v26, 0, v26, s[64:65]
	v_cndmask_b32_e64 v27, 0, v27, s[66:67]
	v_cvt_pkrtz_f16_f32 v34, v24, v25
	v_cvt_pkrtz_f16_f32 v35, v26, v27
	ds_write2_b64 v6, v[32:33], v[34:35] offset0:132 offset1:198
	ds_write_b128 v9, v[168:171] offset:32768
	ds_write_b128 v9, v[172:175] offset:33792
	ds_write_b128 v9, v[176:179] offset:34816
	ds_write_b128 v9, v[180:183] offset:35840
	s_waitcnt lgkmcnt(0)
	s_barrier
	ds_read_b128 v[184:187], v7 offset:33792
	ds_read_b128 v[200:203], v8 offset:32768
	ds_read_b128 v[204:207], v8 offset:33792
	ds_read_b128 v[188:191], v7 offset:33824
	ds_read_b128 v[208:211], v8 offset:34816
	ds_read_b128 v[212:215], v8 offset:35840
	ds_read_b128 v[192:195], v7 offset:33856
	ds_read_b128 v[216:219], v8 offset:36864
	ds_read_b128 v[220:223], v8 offset:37888
	ds_read_b128 v[196:199], v7 offset:33888
	ds_read_b128 v[224:227], v8 offset:38912
	ds_read_b128 v[228:231], v8 offset:39936
	s_waitcnt lgkmcnt(0)
	v_mfma_f32_32x32x16_f16 v[40:55], v[184:187], v[200:203], v[40:55]
	v_mfma_f32_32x32x16_f16 v[56:71], v[184:187], v[204:207], v[56:71]
	v_mfma_f32_32x32x16_f16 v[72:87], v[184:187], v[12:15], v[72:87]
	v_mfma_f32_32x32x16_f16 v[40:55], v[188:191], v[208:211], v[40:55]
	v_mfma_f32_32x32x16_f16 v[56:71], v[188:191], v[212:215], v[56:71]
	v_mfma_f32_32x32x16_f16 v[72:87], v[188:191], v[12:15], v[72:87]
	v_mfma_f32_32x32x16_f16 v[40:55], v[192:195], v[216:219], v[40:55]
	v_mfma_f32_32x32x16_f16 v[56:71], v[192:195], v[220:223], v[56:71]
	v_mfma_f32_32x32x16_f16 v[72:87], v[192:195], v[12:15], v[72:87]
	v_mfma_f32_32x32x16_f16 v[40:55], v[196:199], v[224:227], v[40:55]
	v_mfma_f32_32x32x16_f16 v[56:71], v[196:199], v[228:231], v[56:71]
	v_mfma_f32_32x32x16_f16 v[72:87], v[196:199], v[12:15], v[72:87]
	s_nop 15
	s_barrier
	s_mul_i32 s3, s20, 0xc000
	s_mul_i32 s57, s21, 0xc00
	s_add_u32 s3, s3, s57
	v_add_u32_e32 v36, s3, v1
	ds_write_b128 v36, v[40:43] offset:0
	ds_write_b128 v36, v[56:59] offset:1024
	ds_write_b128 v36, v[72:75] offset:2048
	ds_write_b128 v36, v[44:47] offset:12288
	ds_write_b128 v36, v[60:63] offset:13312
	ds_write_b128 v36, v[76:79] offset:14336
	ds_write_b128 v36, v[48:51] offset:24576
	ds_write_b128 v36, v[64:67] offset:25600
	ds_write_b128 v36, v[80:83] offset:26624
	ds_write_b128 v36, v[52:55] offset:36864
	ds_write_b128 v36, v[68:71] offset:37888
	ds_write_b128 v36, v[84:87] offset:38912
	s_waitcnt lgkmcnt(0)
	s_barrier
	s_mul_i32 s3, s16, 0x3000
	v_add_u32_e32 v36, s3, v1
	ds_read_b128 v[40:43], v36 offset:0
	ds_read_b128 v[44:47], v36 offset:1024
	ds_read_b128 v[48:51], v36 offset:2048
	ds_read_b128 v[52:55], v36 offset:3072
	ds_read_b128 v[56:59], v36 offset:4096
	ds_read_b128 v[60:63], v36 offset:5120
	ds_read_b128 v[64:67], v36 offset:6144
	ds_read_b128 v[68:71], v36 offset:7168
	ds_read_b128 v[72:75], v36 offset:8192
	ds_read_b128 v[76:79], v36 offset:9216
	ds_read_b128 v[80:83], v36 offset:10240
	ds_read_b128 v[84:87], v36 offset:11264
	s_waitcnt lgkmcnt(0)
	v_add_f32_e32 v40, v40, v52
	v_add_f32_e32 v41, v41, v53
	v_add_f32_e32 v42, v42, v54
	v_add_f32_e32 v43, v43, v55
	v_add_f32_e32 v44, v44, v56
	v_add_f32_e32 v45, v45, v57
	v_add_f32_e32 v46, v46, v58
	v_add_f32_e32 v47, v47, v59
	v_add_f32_e32 v48, v48, v60
	v_add_f32_e32 v49, v49, v61
	v_add_f32_e32 v50, v50, v62
	v_add_f32_e32 v51, v51, v63
	v_add_f32_e32 v40, v40, v64
	v_add_f32_e32 v41, v41, v65
	v_add_f32_e32 v42, v42, v66
	v_add_f32_e32 v43, v43, v67
	v_add_f32_e32 v44, v44, v68
	v_add_f32_e32 v45, v45, v69
	v_add_f32_e32 v46, v46, v70
	v_add_f32_e32 v47, v47, v71
	v_add_f32_e32 v48, v48, v72
	v_add_f32_e32 v49, v49, v73
	v_add_f32_e32 v50, v50, v74
	v_add_f32_e32 v51, v51, v75
	v_add_f32_e32 v40, v40, v76
	v_add_f32_e32 v41, v41, v77
	v_add_f32_e32 v42, v42, v78
	v_add_f32_e32 v43, v43, v79
	v_add_f32_e32 v44, v44, v80
	v_add_f32_e32 v45, v45, v81
	v_add_f32_e32 v46, v46, v82
	v_add_f32_e32 v47, v47, v83
	v_add_f32_e32 v48, v48, v84
	v_add_f32_e32 v49, v49, v85
	v_add_f32_e32 v50, v50, v86
	v_add_f32_e32 v51, v51, v87
	v_cmp_eq_f32_e64 s[60:61], 0, v48
	v_cmp_eq_f32_e64 s[62:63], 0, v49
	v_cmp_eq_f32_e64 s[64:65], 0, v50
	v_cmp_eq_f32_e64 s[66:67], 0, v51
	s_nop 3
	s_or_b64 s[60:61], s[60:61], s[62:63]
	s_or_b64 s[64:65], s[64:65], s[66:67]
	s_or_b64 s[60:61], s[60:61], s[64:65]
	s_cmp_eq_u64 s[60:61], 0
	s_cbranch_scc1 .Lgm_no_fallback
	v_and_b32_e32 v101, 31, v2
	v_lshlrev_b32_e32 v101, 4, v101
	v_mov_b32_e32 v88, 0
	v_mov_b32_e32 v89, 0
	s_mov_b32 s3, 0
